# K-tile LDS-DMA pieces use a scalar base plus fixed 32-bit lane offsets; one instruction kept between every m0 write and its LDS-DMA
# speedup vs baseline: 1.0094x; 1.0042x over previous
; DEVI int tidx() { int t = threadIdx.x; asm volatile("" : "+v"(t)); __builtin_assume(t >= 0 && t < 512); return t; }
; DEVI unsigned cvt_pk_bf16(float lo, float hi) { unsigned r; asm volatile("v_cvt_pk_bf16_f32 %0, %1, %2" : "=v"(r) : "v"(lo), "v"(hi)); return r; }
; DEVI float bf2f(bf16_t h) { return __uint_as_float(((unsigned)h) << 16); }
; DEVI void attn_unit8(const Params& p, char* smem, int unit, int l, int& cvs  , CvRun& crun) {
;     const int tid = tidx(), wid = __builtin_amdgcn_readfirstlane(tid >> 6), lane = tid & 63, r32 = lane & 31, hi = lane >> 5;
;     const int x8 = unit & 7, v8 = unit >> 3, bh = x8 + 8 * (v8 >> 4), qt = v8 & 15, b = bh >> 3, hh = bh & 7;
;     char* K_lds = smem; char* V_lds = smem + 73728;
;     float* wsx = (float*)(smem + 122880) + wid * 64; float* li_l = wsx; float* al_l = wsx + 32;
;     const bf16_t* Kg = p.kfull + (size_t)bh * S_ * 96; const bf16_t* Vg = p.vfull + (size_t)bh * S_ * 64;
;     const size_t qtok = (size_t)b * S_ + qt * 256 + wid * 32 + r32;
;     bf16x8 qr[6];
;     { const bf16_t* qp = p.qbuf + qtok * 768 + hh * 96 + hi * 8;
; #pragma unroll
;       for (int d0 = 0; d0 < 6; ++d0) qr[d0] = *(const bf16x8*)(qp + d0 * 16);
;       const f32x4 c0 = *(const f32x4*)(p.cs + qtok * 16 + hi * 8), c1 = *(const f32x4*)(p.cs + qtok * 16 + hi * 8 + 4);
;       const f32x4 s0 = *(const f32x4*)(p.sn + qtok * 16 + hi * 8), s1 = *(const f32x4*)(p.sn + qtok * 16 + hi * 8 + 4);
;       float o1[8], o2[8];
; #pragma unroll
;       for (int j = 0; j < 8; ++j) { const float x1 = bf2f((bf16_t)qr[4][j]), x2 = bf2f((bf16_t)qr[5][j]); const float cc = j < 4 ? c0[j] : c1[j - 4], ss = j < 4 ? s0[j] : s1[j - 4];
;           o1[j] = x1 * cc - x2 * ss; o2[j] = x2 * cc + x1 * ss; }
;       u32x4 w1, w2;
; #pragma unroll
;       for (int j = 0; j < 4; ++j) { w1[j] = cvt_pk_bf16(o1[2 * j], o1[2 * j + 1]); w2[j] = cvt_pk_bf16(o2[2 * j], o2[2 * j + 1]); }
;       qr[4] = *(bf16x8*)&w1; qr[5] = *(bf16x8*)&w2; }
;     int ksrc[3];
; #pragma unroll
;     for (int i = 0; i < 3; ++i) { const int pc = tid + 512 * i, row = pc / 12, ch = (pc % 12) ^ ((row >> 2) & 3); ksrc[i] = row * 192 + ch * 16; }
.LBB0_665:
	v_mov_b32_e32 v86, v0
	s_ashr_i32 s5, s83, 4
	v_readfirstlane_b32 s4, v86
	s_lshr_b32 s53, s4, 6
	s_and_b32 s52, s5, -8
	s_and_b32 s8, s4, 0x3fffffc0
	s_load_dwordx4 s[4:7], s[24:25], 0x1a0
	s_load_dwordx4 s[12:15], s[24:25], 0x110
	s_and_b32 s87, s83, 7
	s_ashr_i32 s16, s83, 7
	s_lshl_b32 s8, s8, 2
	s_or_b32 s10, s52, s87
	s_add_i32 s91, s8, 0
	s_ashr_i32 s17, s16, 31
	s_lshl_b32 s8, s83, 5
	s_ashr_i32 s11, s10, 31
	s_lshl_b64 s[16:17], s[16:17], 12
	s_and_b32 s8, s8, 0xf00
	s_and_b32 s2, s62, 7
	s_add_i32 s91, s91, 0x1e000
	s_waitcnt lgkmcnt(0)
	v_mov_b32_e32 v2, s4
	v_mov_b32_e32 v3, s5
	s_lshl_b64 s[4:5], s[10:11], 19
	s_or_b32 s8, s16, s8
	s_lshl_b32 s11, s53, 5
	v_and_b32_e32 v176, 31, v86
	s_add_u32 s48, s8, s11
	v_or_b32_e32 v10, s48, v176
	s_movk_i32 s8, 0x600
	s_addc_u32 s49, s17, 0
	v_mad_u64_u32 v[2:3], s[16:17], v10, s8, v[2:3]
	v_bfe_u32 v186, v86, 5, 1
	v_mad_i32_i24 v3, s49, v177, v3
	s_mul_i32 s8, s87, 0xc0
	v_mov_b32_e32 v11, s49
	v_lshl_add_u64 v[2:3], v[2:3], 0, s[8:9]
	v_lshlrev_b32_e32 v178, 4, v186
	v_mov_b32_e32 v179, v175
	v_lshl_add_u64 v[26:27], v[2:3], 0, v[178:179]
	v_lshlrev_b64 v[10:11], 6, v[10:11]
	global_load_dwordx4 v[2:5], v[26:27], off offset:128
	global_load_dwordx4 v[6:9], v[26:27], off offset:160
	v_lshl_add_u64 v[12:13], s[12:13], 0, v[10:11]
	v_and_b32_e32 v174, 32, v86
	v_lshl_add_u64 v[10:11], s[14:15], 0, v[10:11]
	v_lshl_add_u64 v[22:23], v[12:13], 0, v[174:175]
	v_lshl_add_u64 v[18:19], v[10:11], 0, v[174:175]
	global_load_dwordx4 v[10:13], v[18:19], off
	global_load_dwordx4 v[14:17], v[22:23], off
	s_nop 0
	global_load_dwordx4 v[18:21], v[18:19], off offset:16
	s_nop 0
	global_load_dwordx4 v[22:25], v[22:23], off offset:16
	s_load_dwordx2 s[50:51], s[24:25], 0x1b0
	global_load_dwordx4 v[150:153], v[26:27], off
	global_load_dwordx4 v[138:141], v[26:27], off offset:32
	global_load_dwordx4 v[134:137], v[26:27], off offset:64
	global_load_dwordx4 v[130:133], v[26:27], off offset:96
	s_mul_hi_i32 s8, s10, 0xc0000
	s_mul_i32 s10, s10, 0xc0000
	s_add_u32 s10, s6, s10
	s_addc_u32 s11, s7, s8
	s_lshl_b32 s61, s53, 10
	s_add_i32 s96, s61, 0
	s_waitcnt lgkmcnt(0)
	s_add_u32 s4, s50, s4
	s_mov_b32 m0, s96
	v_lshlrev_b32_e32 v88, 6, v186
	s_addc_u32 s5, s51, s5
	s_add_i32 s97, s75, s61
	v_lshlrev_b32_e32 v90, 2, v86
	v_and_b32_e32 v91, 63, v86
	v_lshlrev_b32_e32 v93, 4, v91
	v_lshlrev_b32_e32 v92, 3, v91
	v_lshlrev_b32_e32 v94, 1, v91
	s_mov_b32 s8, s9
	s_mov_b32 s12, s9
	s_mov_b32 s13, s9
	s_mov_b32 s14, s9
	s_mov_b32 s15, s9
	s_mov_b32 s16, s9
	s_mov_b32 s17, s9
	s_mov_b32 s18, s9
	s_mov_b32 s19, s9
	s_mov_b32 s20, s9
	s_mov_b32 s21, s9
	s_mov_b32 s22, s9
	s_mov_b32 s23, s9
	s_mulk_i32 s53, 0x900
	v_mov_b32_e32 v83, v175
	v_mov_b32_e32 v85, v175
	v_and_b32_e32 v114, 28, v90
	v_lshl_add_u32 v187, v176, 2, s91
	v_mul_u32_u24_e32 v201, 0x44, v114
	v_bfe_u32 v195, v91, 1, 2
	v_mov_b32_e32 v207, 1.0
	s_mov_b32 s89, s9
	v_mov_b32_e32 v188, v175
	s_waitcnt vmcnt(9)
	v_lshlrev_b32_e32 v27, 16, v2
	s_waitcnt vmcnt(8)
	v_lshlrev_b32_e32 v26, 16, v6
	v_and_b32_e32 v33, 0xffff0000, v2
	v_lshlrev_b32_e32 v35, 16, v3
	s_waitcnt vmcnt(7)
	v_mov_b32_e32 v28, v10
	s_waitcnt vmcnt(6)
	v_mov_b32_e32 v29, v14
	v_mov_b32_e32 v36, v12
	v_mov_b32_e32 v37, v16
	v_mov_b32_e32 v38, v16
	v_mov_b32_e32 v39, v12
	v_and_b32_e32 v3, 0xffff0000, v3
	v_and_b32_e32 v2, 0xffff0000, v7
	v_mov_b32_e32 v16, v13
	v_mov_b32_e32 v12, v17
	v_and_b32_e32 v32, 0xffff0000, v6
	v_lshlrev_b32_e32 v34, 16, v7
	v_pk_mul_f32 v[6:7], v[28:29], v[26:27]
	v_pk_mul_f32 v[16:17], v[16:17], v[2:3]
	v_pk_mul_f32 v[2:3], v[12:13], v[2:3]
	v_mov_b32_e32 v30, v14
	v_mov_b32_e32 v31, v10
	v_sub_f32_e32 v12, v7, v6
	v_sub_f32_e32 v16, v17, v16
	v_add_f32_e32 v17, v2, v3
	v_lshlrev_b32_e32 v3, 16, v4
	v_lshlrev_b32_e32 v2, 16, v8
	s_waitcnt vmcnt(5)
	v_mov_b32_e32 v6, v18
	s_waitcnt vmcnt(4)
	v_mov_b32_e32 v7, v22
	v_pk_mul_f32 v[26:27], v[30:31], v[26:27]
	v_pk_mul_f32 v[6:7], v[6:7], v[2:3]
	v_add_f32_e32 v13, v26, v27
	v_sub_f32_e32 v26, v7, v6
	v_mov_b32_e32 v6, v22
	v_mov_b32_e32 v7, v18
	v_pk_mul_f32 v[2:3], v[6:7], v[2:3]
	v_mov_b32_e32 v22, v19
	v_add_f32_e32 v27, v2, v3
	v_and_b32_e32 v3, 0xffff0000, v4
	v_and_b32_e32 v2, 0xffff0000, v8
	v_mov_b32_e32 v18, v23
	v_pk_mul_f32 v[6:7], v[22:23], v[2:3]
	v_pk_mul_f32 v[2:3], v[18:19], v[2:3]
	v_sub_f32_e32 v8, v7, v6
	v_add_f32_e32 v18, v2, v3
	v_lshlrev_b32_e32 v3, 16, v5
	v_lshlrev_b32_e32 v2, 16, v9
	v_mov_b32_e32 v6, v20
	v_mov_b32_e32 v7, v24
	v_pk_mul_f32 v[6:7], v[6:7], v[2:3]
	v_mov_b32_e32 v14, v11
	v_sub_f32_e32 v19, v7, v6
	v_mov_b32_e32 v6, v24
	v_mov_b32_e32 v7, v20
	v_pk_mul_f32 v[2:3], v[6:7], v[2:3]
	v_mov_b32_e32 v24, v21
	v_add_f32_e32 v6, v2, v3
	v_and_b32_e32 v3, 0xffff0000, v5
	v_and_b32_e32 v2, 0xffff0000, v9
	v_mov_b32_e32 v20, v25
	v_mov_b32_e32 v10, v15
	v_pk_mul_f32 v[4:5], v[24:25], v[2:3]
	v_pk_mul_f32 v[2:3], v[20:21], v[2:3]
	v_pk_mul_f32 v[14:15], v[14:15], v[32:33]
	v_pk_mul_f32 v[10:11], v[10:11], v[32:33]
	v_pk_mul_f32 v[28:29], v[36:37], v[34:35]
	v_pk_mul_f32 v[30:31], v[38:39], v[34:35]
	v_add_f32_e32 v2, v2, v3
	v_sub_f32_e32 v14, v15, v14
	v_add_f32_e32 v10, v10, v11
	v_sub_f32_e32 v11, v29, v28
	v_add_f32_e32 v15, v30, v31
	v_sub_f32_e32 v4, v5, v4
	v_cvt_pk_bf16_f32 v146, v12, v14
	v_cvt_pk_bf16_f32 v142, v13, v10
	v_cvt_pk_bf16_f32 v147, v11, v16
	v_cvt_pk_bf16_f32 v143, v15, v17
	v_cvt_pk_bf16_f32 v148, v26, v8
	v_cvt_pk_bf16_f32 v144, v27, v18
	v_cvt_pk_bf16_f32 v149, v19, v4
	v_cvt_pk_bf16_f32 v145, v6, v2
	v_mul_u32_u24_e32 v2, 0xaaab, v86
	v_lshrrev_b32_e32 v3, 19, v2
	v_mul_lo_u16_e32 v4, 12, v3
	v_sub_u16_e32 v4, v86, v4
	v_lshrrev_b32_e32 v2, 21, v2
; #define LAS __attribute__((address_space(3)))
; DEVI int v_rd_base(int lane) { return ((lane & 3) << 3) | (((lane >> 2) & 3) << 6) | (((lane >> 4) & 1) << 5) | (((lane >> 5) & 1) << 8); }
; #define VM0() asm volatile("s_waitcnt vmcnt(0)" ::: "memory")
; DEVI void attn_unit8(const Params& p, char* smem, int unit, int l, int& cvs  , CvRun& crun) {
;     ...
;     for (int i = 0; i < 3; ++i) { const int pc = tid + 512 * i, row = pc / 12, ch = (pc % 12) ^ ((row >> 2) & 3); ksrc[i] = row * 192 + ch * 16; }
;     const int vsrc = wid * 1024 + ((lane >> 2) & 7) * 128 + (lane >> 5) * 64 + (lane & 3) * 16;
;     LAS char* const Kl = (LAS char*)K_lds + wid * 1024; LAS char* const Vl = (LAS char*)V_lds + wid * 1024;
;     ...
;     const int vb0 = (int)(uintptr_t)(LAS char*)V_lds + v_rd_base(lane);
;     float m_reg = 0.f, l_reg = 0.f; f32x16 o[2];
; #pragma unroll
;     for (int d = 0; d < 2; ++d)
; #pragma unroll
;         for (int r = 0; r < 16; ++r) o[d][r] = 0.f;
;     f32x16 pA0, pA1, pB0, pB1; float alA, alB; bf16x8 pa0, pa1, pa2, pa3;
;     constexpr int NTILE = S_ / 128;
;     B_DMA(0, 0); B_DMA(1, 1); VM0(); __syncthreads();
	v_bitop3_b32 v2, v2, v4, 3 bitop3:0x6c
	v_mul_u32_u24_e32 v3, 0xc0, v3
	v_lshl_add_u32 v174, v2, 4, v3
	v_or_b32_e32 v2, 0x200, v86
	v_mul_u32_u24_sdwa v3, v2, s74 dst_sel:DWORD dst_unused:UNUSED_PAD src0_sel:WORD_0 src1_sel:DWORD
	v_lshrrev_b32_e32 v4, 19, v3
	v_mul_lo_u16_e32 v5, 12, v4
	v_sub_u16_e32 v2, v2, v5
	v_lshrrev_b32_e32 v3, 21, v3
	v_bitop3_b32 v2, v3, v2, 3 bitop3:0x6c
	v_mul_u32_u24_e32 v3, 0xc0, v4
	v_lshl_add_u32 v82, v2, 4, v3
	v_or_b32_e32 v2, 0x400, v86
	v_mul_u32_u24_sdwa v3, v2, s74 dst_sel:DWORD dst_unused:UNUSED_PAD src0_sel:WORD_0 src1_sel:DWORD
	v_lshrrev_b32_e32 v4, 19, v3
	v_mul_lo_u16_e32 v5, 12, v4
	v_sub_u16_e32 v2, v2, v5
	v_lshrrev_b32_e32 v3, 21, v3
	v_bitop3_b32 v2, v3, v2, 3 bitop3:0x6c
	v_mul_u32_u24_e32 v3, 0xc0, v4
	v_lshl_add_u32 v84, v2, 4, v3
	v_lshlrev_b32_e32 v2, 5, v86
	v_and_b32_e32 v87, 0x380, v2
	v_lshlrev_b32_e32 v3, 4, v86
	global_load_lds_dwordx4 v174, s[10:11]
	s_add_i32 m0, s96, 0x2000
	v_or_b32_e32 v2, v88, v87
	v_and_b32_e32 v89, 48, v3
	global_load_lds_dwordx4 v82, s[10:11]
	s_add_i32 m0, s96, 0x4000
	v_or3_b32 v2, v2, v89, s61
	global_load_lds_dwordx4 v84, s[10:11]
	v_mov_b32_e32 v3, v175
	s_mov_b32 m0, s97
	v_lshl_add_u64 v[4:5], s[4:5], 0, v[2:3]
	global_load_lds_dwordx4 v2, s[4:5]
	s_add_i32 m0, s97, 0x2000
	v_lshl_add_u64 v[2:3], v[4:5], 0, s[40:41]
	s_add_u32 s4, s10, 0x6000
	global_load_lds_dwordx4 v[2:3], off
	s_addc_u32 s5, s11, 0
	s_add_i32 m0, s96, 0x6000
	v_lshl_add_u64 v[2:3], v[4:5], 0, s[44:45]
	global_load_lds_dwordx4 v174, s[4:5]
	s_add_i32 m0, s96, 0x8000
	v_mul_u32_u24_e32 v10, 0xc0, v176
	global_load_lds_dwordx4 v82, s[4:5]
	s_add_i32 m0, s96, 0xa000
	v_and_b32_e32 v11, 48, v90
	global_load_lds_dwordx4 v84, s[4:5]
	s_add_i32 m0, s97, 0x4000
	v_bitop3_b32 v129, v178, v10, v11 bitop3:0xde
	global_load_lds_dwordx4 v[2:3], off
	v_lshl_add_u64 v[2:3], v[4:5], 0, s[42:43]
	s_add_i32 m0, s97, 0x6000
	v_add_u32_e32 v189, 0, v129
	global_load_lds_dwordx4 v[2:3], off
	s_waitcnt vmcnt(0)
	s_waitcnt vmcnt(0) lgkmcnt(0)
	s_barrier
; #define VM0() asm volatile("s_waitcnt vmcnt(0)" ::: "memory")
; #define C_SPLAT() do { _Pragma("unroll") for (int _r = 0; _r < 16; ++_r) cinit[_r] = -m_reg; asm volatile("" : "+v"(cinit)); } while (0)
; template <bool FIRST> DEVI bool partialSM(f32x16& p0, f32x16& p1, float& m_reg, float& alpha) {
;     float pmax = p0[0];
; #pragma unroll
;     for (int r = 1; r < 16; ++r) pmax = fmaxf(pmax, p0[r]);
; #pragma unroll
;     for (int r = 0; r < 16; ++r) pmax = fmaxf(pmax, p1[r]);
;     { auto rr = __builtin_amdgcn_permlane32_swap(__float_as_uint(pmax), __float_as_uint(pmax), false, false);
;       pmax = fmaxf(__uint_as_float(rr[0]), __uint_as_float(rr[1])); }
;     if (FIRST) { m_reg = pmax; alpha = 1.f;
; #pragma unroll
;         for (int r = 0; r < 16; ++r) { p0[r] = __builtin_amdgcn_exp2f(p0[r] - pmax); p1[r] = p1[r] - pmax; }
;         return false;
; DEVI void attn_unit8(const Params& p, char* smem, int unit, int l, int& cvs  , CvRun& crun) {
;     ...
;     float m_reg = 0.f, l_reg = 0.f; f32x16 o[2];
; #pragma unroll
;     for (int d = 0; d < 2; ++d)
; #pragma unroll
;         for (int r = 0; r < 16; ++r) o[d][r] = 0.f;
;     f32x16 pA0, pA1, pB0, pB1; float alA, alB; bf16x8 pa0, pa1, pa2, pa3;
;     constexpr int NTILE = S_ / 128;
;     B_DMA(0, 0); B_DMA(1, 1); VM0(); __syncthreads();
;     f32x16 cinit;
;     ...
;     { f32x16 z; _Pragma("unroll") for (int r = 0; r < 16; ++r) z[r] = 0.f;
;       qkt(pA0, pA1, K_lds, qr, r32, hi, z); } partialSM<true>(pA0, pA1, m_reg, alA); C_SPLAT();
;     int s0 = 0, s1 = 1, s2 = 2;
	ds_read_b128 v[2:5], v189
	ds_read_b128 v[6:9], v189 offset:6144
	s_waitcnt lgkmcnt(1)
	v_mfma_f32_32x32x16_bf16 v[34:49], v[2:5], v[150:153], 0
	v_or_b32_e32 v2, 32, v178
	v_bitop3_b32 v184, v2, v10, v11 bitop3:0xde
	v_add_u32_e32 v190, 0, v184
	s_mov_b32 s10, s9
	s_mov_b32 s11, s9
	s_lshl_b32 s71, s54, 5
	s_lshl_b32 s84, s54, 4
	s_waitcnt lgkmcnt(0)
	v_mfma_f32_32x32x16_bf16 v[18:33], v[6:9], v[150:153], 0
	ds_read_b128 v[2:5], v190
	ds_read_b128 v[6:9], v190 offset:6144
	s_lshl_b32 s85, s54, 3
	s_lshl_b32 s88, s54, 1
	v_cmp_gt_u32_e64 s[4:5], 32, v91
	s_waitcnt lgkmcnt(1)
	v_mfma_f32_32x32x16_bf16 v[34:49], v[2:5], v[138:141], v[34:49]
	v_or_b32_e32 v2, 64, v178
	v_xad_u32 v185, v2, v11, v10
	v_add_u32_e32 v191, 0, v185
	s_waitcnt lgkmcnt(0)
	v_mfma_f32_32x32x16_bf16 v[18:33], v[6:9], v[138:141], v[18:33]
	ds_read_b128 v[2:5], v191
	ds_read_b128 v[6:9], v191 offset:6144
	s_waitcnt lgkmcnt(1)
	v_mfma_f32_32x32x16_bf16 v[34:49], v[2:5], v[134:137], v[34:49]
	v_or_b32_e32 v2, 0x60, v178
	v_xad_u32 v204, v2, v11, v10
	v_add_u32_e32 v192, 0, v204
	ds_read_b128 v[2:5], v192
	s_waitcnt lgkmcnt(1)
	v_mfma_f32_32x32x16_bf16 v[18:33], v[6:9], v[134:137], v[18:33]
	ds_read_b128 v[6:9], v192 offset:6144
	s_waitcnt lgkmcnt(1)
	v_mfma_f32_32x32x16_bf16 v[34:49], v[2:5], v[130:133], v[34:49]
	v_and_b32_e32 v2, 0xc0, v93
	v_and_or_b32 v12, v92, 24, v2
	v_or_b32_e32 v2, 0x80, v178
	v_xad_u32 v205, v2, v11, v10
	v_add_u32_e32 v193, 0, v205
	ds_read_b128 v[2:5], v193
	s_waitcnt lgkmcnt(1)
	v_mfma_f32_32x32x16_bf16 v[18:33], v[6:9], v[130:133], v[18:33]
	v_and_b32_e32 v6, 32, v94
	v_and_b32_e32 v7, 0x100, v92
	v_or3_b32 v179, v12, v6, v7
	ds_read_b128 v[6:9], v193 offset:6144
	v_add_u32_e32 v115, s75, v179
	s_waitcnt lgkmcnt(1)
	v_mfma_f32_32x32x16_bf16 v[34:49], v[2:5], v[146:149], v[34:49]
	v_or_b32_e32 v2, 0xa0, v178
	v_xad_u32 v206, v2, v11, v10
	v_add_u32_e32 v194, 0, v206
	ds_read_b128 v[2:5], v194
	ds_read_b128 v[50:53], v194 offset:6144
	s_waitcnt lgkmcnt(2)
	v_mfma_f32_32x32x16_bf16 v[18:33], v[6:9], v[146:149], v[18:33]
	s_waitcnt lgkmcnt(1)
	v_mfma_f32_32x32x16_bf16 v[34:49], v[2:5], v[142:145], v[34:49]
	v_mov_b64_e32 v[2:3], s[8:9]
	v_mov_b64_e32 v[4:5], s[10:11]
	v_mov_b64_e32 v[6:7], s[12:13]
	v_mov_b64_e32 v[8:9], s[14:15]
	v_mov_b64_e32 v[10:11], s[16:17]
	v_mov_b64_e32 v[12:13], s[18:19]
	v_mov_b64_e32 v[14:15], s[20:21]
	s_waitcnt lgkmcnt(0)
	v_mfma_f32_32x32x16_bf16 v[18:33], v[50:53], v[142:145], v[18:33]
	s_nop 2
	v_max_f32_e32 v50, v35, v35
	v_max_f32_e32 v51, v34, v34
	v_max_f32_e32 v50, v51, v50
	v_max3_f32 v50, v50, v36, v37
	v_max3_f32 v50, v50, v38, v39
	v_max3_f32 v50, v50, v40, v41
	v_max3_f32 v50, v50, v42, v43
	v_max3_f32 v50, v50, v44, v45
	v_max3_f32 v50, v50, v46, v47
	v_max3_f32 v50, v50, v48, v49
	v_max3_f32 v50, v50, v18, v19
	v_max3_f32 v50, v50, v20, v21
	v_max3_f32 v50, v50, v22, v23
	v_max3_f32 v50, v50, v24, v25
	v_max3_f32 v50, v50, v26, v27
	v_max3_f32 v50, v50, v28, v29
	v_max3_f32 v50, v50, v30, v31
	v_max3_f32 v50, v50, v32, v33
	v_mov_b32_e32 v51, v50
	s_nop 1
	v_permlane32_swap_b32_e32 v50, v51
	v_max_f32_e32 v51, v51, v51
	v_max_f32_e32 v50, v50, v50
	v_max_f32_e32 v203, v50, v51
	v_sub_f32_e32 v34, v34, v203
	v_exp_f32_e32 v50, v34
	v_sub_f32_e32 v34, v35, v203
	v_exp_f32_e32 v51, v34
	v_sub_f32_e32 v34, v36, v203
	v_exp_f32_e32 v52, v34
	v_sub_f32_e32 v34, v37, v203
	v_exp_f32_e32 v53, v34
	v_sub_f32_e32 v34, v38, v203
	v_exp_f32_e32 v54, v34
	v_sub_f32_e32 v34, v39, v203
	v_exp_f32_e32 v55, v34
	v_sub_f32_e32 v34, v40, v203
	v_exp_f32_e32 v56, v34
	v_sub_f32_e32 v34, v41, v203
	v_exp_f32_e32 v57, v34
	v_sub_f32_e32 v34, v42, v203
	v_mov_b64_e32 v[16:17], s[22:23]
	v_exp_f32_e32 v58, v34
	v_sub_f32_e32 v34, v43, v203
	v_sub_f32_e32 v67, v19, v203
	s_add_i32 s8, s53, 0
	v_bfe_u32 v19, v86, 1, 5
	v_exp_f32_e32 v59, v34
	v_sub_f32_e32 v34, v44, v203
	v_sub_f32_e32 v68, v20, v203
	s_add_i32 s8, s8, 0x1e800
	v_and_b32_e32 v20, 28, v19
	s_or_b32 s10, s52, s2
	v_exp_f32_e32 v60, v34
	v_sub_f32_e32 v34, v45, v203
	v_sub_f32_e32 v69, v21, v203
	v_add_u32_e32 v200, s8, v20
	v_mov_b32_e32 v21, s8
	s_lshl_b32 s8, s54, 10
	s_ashr_i32 s11, s10, 31
	v_exp_f32_e32 v61, v34
	v_sub_f32_e32 v34, v46, v203
	s_add_i32 s70, s8, 0xf7f80000
	s_lshl_b64 s[12:13], s[10:11], 19
	v_exp_f32_e32 v62, v34
	v_sub_f32_e32 v34, v47, v203
	v_sub_f32_e32 v66, v18, v203
	v_lshrrev_b32_e32 v18, 2, v86
	s_add_u32 s12, s50, s12
	v_exp_f32_e32 v63, v34
	v_sub_f32_e32 v34, v48, v203
	v_sub_f32_e32 v70, v22, v203
	v_and_b32_e32 v128, 14, v18
	v_lshrrev_b32_e32 v22, 3, v86
	v_and_b32_e32 v18, 12, v18
	s_addc_u32 s13, s51, s13
	s_mul_i32 s8, s10, 0xc0000
	v_exp_f32_e32 v64, v34
	v_sub_f32_e32 v34, v49, v203
	v_mad_u32_u24 v198, v19, s77, v21
	v_and_b32_e32 v19, 0x80, v92
	v_and_b32_e32 v21, 16, v94
	v_and_b32_e32 v22, 4, v22
	v_and_or_b32 v197, v93, s76, v18
	v_or_b32_e32 v18, s61, v87
	s_mul_hi_i32 s2, s10, 0xc0000
	s_add_u32 s6, s6, s8
	v_exp_f32_e32 v65, v34
	v_or3_b32 v196, v19, v22, v21
	v_or3_b32 v18, v18, v88, v89
	v_mov_b32_e32 v19, v175
	s_addc_u32 s2, s7, s2
	v_and_b32_e32 v20, 1, v86
	v_lshl_add_u64 v[18:19], s[12:13], 0, v[18:19]
	s_add_u32 s6, s6, 0xc000
	v_xor_b32_e32 v34, 0x80000000, v203
	v_sub_f32_e32 v81, v33, v203
	v_sub_f32_e32 v80, v32, v203
	v_sub_f32_e32 v79, v31, v203
	v_sub_f32_e32 v78, v30, v203
	v_sub_f32_e32 v77, v29, v203
	v_sub_f32_e32 v76, v28, v203
	v_sub_f32_e32 v75, v27, v203
	v_sub_f32_e32 v74, v26, v203
	v_sub_f32_e32 v73, v25, v203
	v_sub_f32_e32 v72, v24, v203
	v_sub_f32_e32 v71, v23, v203
	v_lshlrev_b32_e32 v199, 5, v20
	v_lshlrev_b32_e32 v180, 4, v20
	v_lshl_add_u64 v[116:117], v[18:19], 0, s[46:47]
	s_addc_u32 s7, s2, 0
	v_mov_b64_e32 v[32:33], v[16:17]
	v_mov_b32_e32 v35, v34
	v_mov_b32_e32 v36, v34
	v_mov_b32_e32 v37, v34
	v_mov_b32_e32 v38, v34
	v_mov_b32_e32 v39, v34
	v_mov_b32_e32 v40, v34
	v_mov_b32_e32 v41, v34
	v_mov_b32_e32 v42, v34
	v_mov_b32_e32 v43, v34
	v_mov_b32_e32 v44, v34
	v_mov_b32_e32 v45, v34
	v_mov_b32_e32 v46, v34
	v_mov_b32_e32 v47, v34
	v_mov_b32_e32 v48, v34
	v_mov_b32_e32 v49, v34
	v_mov_b32_e32 v118, v174
	v_mov_b32_e32 v120, v82
	v_mov_b32_e32 v122, v84
	s_mov_b64 s[12:13], s[6:7]
	s_add_u32 s67, s6, 0xb4000
	v_mov_b64_e32 v[30:31], v[14:15]
	v_mov_b64_e32 v[28:29], v[12:13]
	v_mov_b64_e32 v[26:27], v[10:11]
	v_mov_b64_e32 v[24:25], v[8:9]
	v_mov_b64_e32 v[22:23], v[6:7]
	v_mov_b64_e32 v[20:21], v[4:5]
	v_mov_b64_e32 v[18:19], v[2:3]
	s_mov_b32 s6, 2
	s_mov_b32 s2, 1

; #define VM0() asm volatile("s_waitcnt vmcnt(0)" ::: "memory")
; #define B_RESC(a, rare) do { if (rare) { if (hi == 0) al_l[r32] = (a); asm volatile("s_waitcnt lgkmcnt(0)" ::: "memory"); __builtin_amdgcn_wave_barrier(); \
;         _Pragma("unroll") for (int _d = 0; _d < 2; ++_d) _Pragma("unroll") for (int _r = 0; _r < 16; ++_r) o[_d][_r] *= al_l[crow(_r, hi)]; C_SPLAT(); } } while (0)
; DEVI void attn_unit8(const Params& p, char* smem, int unit, int l, int& cvs  , CvRun& crun) {
;     ...
;     for (int T = 0; T + 1 < NTILE; ++T) {
;         const char* Kb = K_lds + s0 * 24576; const int vb = vb0 + s0 * 16384;
;         CvRegs cvr; cv_issue(p, l, cvs, lane, cvr, crun); cvs += (int)gridDim.x * 8;
;         qkt(pB0, pB1, Kb + 12288, qr, r32, hi, cinit);
;         finishSM(pA0, pA1, alA, l_reg, pa0, pa1, pa2, pa3);
;         pv_both(o[0], o[1], vb, pa0, pa1, pa2, pa3);
;         { const bool rr_ = partialSM<false>(pB0, pB1, m_reg, alB); B_RESC(alB, rr_); }
;         cv_finish(smem + 124928 + wid * 2304, lane, cvr);
;         if (cvr.live) asm volatile("s_waitcnt vmcnt(2)" ::: "memory"); else VM0();
;         __syncthreads();
;         if (T + 2 < NTILE) B_DMA(T + 2, s2);
.LBB0_702:
	s_mul_i32 s98, s2, 0x6000
	s_add_i32 s98, s96, s98
	s_lshl_b32 s99, s2, 14
	s_add_i32 s99, s97, s99
	s_mul_i32 s6, s61, 0x6000
	s_add_i32 s6, s6, 0
	v_add_u32_e32 v249, s6, v129

; #define VM0() asm volatile("s_waitcnt vmcnt(0)" ::: "memory")
; DEVI void attn_unit8(const Params& p, char* smem, int unit, int l, int& cvs  , CvRun& crun) {
;     ...
;         if (cvr.live) asm volatile("s_waitcnt vmcnt(2)" ::: "memory"); else VM0();
;         __syncthreads();
;         if (T + 2 < NTILE) B_DMA(T + 2, s2);
;         qkt(pA0, pA1, K_lds + s1 * 24576, qr, r32, hi, cinit);
	s_mov_b32 m0, s98
	s_barrier
	ds_read_b128 v[234:237], v249
	ds_read_b128 v[210:213], v249 offset:6144
	global_load_lds_dwordx4 v118, s[12:13]
	s_waitcnt lgkmcnt(1)
	v_mfma_f32_32x32x16_bf16 v[98:113], v[234:237], v[150:153], v[34:49]
	s_add_i32 m0, s98, 0x2000

; DEVI void attn_unit8(const Params& p, char* smem, int unit, int l, int& cvs  , CvRun& crun) {
;     ...
;         if (T + 2 < NTILE) B_DMA(T + 2, s2);
;         qkt(pA0, pA1, K_lds + s1 * 24576, qr, r32, hi, cinit);
	v_add_u32_e32 v126, s6, v184
	global_load_lds_dwordx4 v120, s[12:13]
	s_waitcnt lgkmcnt(0)
	v_mfma_f32_32x32x16_bf16 v[66:81], v[210:213], v[150:153], v[34:49]
	ds_read_b128 v[210:213], v126
	ds_read_b128 v[214:217], v126 offset:6144
	s_add_i32 m0, s98, 0x4000

; template <int OFF> DEVI s16x4 tr_read(int vb) { s16x4 r; asm volatile("ds_read_b64_tr_b16 %0, %1 offset:%2" : "=&v"(r) : "v"(vb), "i"(OFF) : "memory"); return r; }
; #define SBAR() __builtin_amdgcn_sched_barrier(0)
; DEVI void pv_both(f32x16& o0, f32x16& o1, int vb, bf16x8 pa0, bf16x8 pa1, bf16x8 pa2, bf16x8 pa3) {
;     const s16x4 a0 = tr_read<v_rd_off(0, 0, 0)>(vb), b0 = tr_read<v_rd_off(0, 0, 1)>(vb), a1 = tr_read<v_rd_off(0, 1, 0)>(vb), b1 = tr_read<v_rd_off(0, 1, 1)>(vb);
;     const s16x4 a2 = tr_read<v_rd_off(0, 2, 0)>(vb), b2 = tr_read<v_rd_off(0, 2, 1)>(vb), a3 = tr_read<v_rd_off(0, 3, 0)>(vb), b3 = tr_read<v_rd_off(0, 3, 1)>(vb);
;     const s16x4 c0 = tr_read<v_rd_off(1, 0, 0)>(vb), d0 = tr_read<v_rd_off(1, 0, 1)>(vb), c1 = tr_read<v_rd_off(1, 1, 0)>(vb), d1 = tr_read<v_rd_off(1, 1, 1)>(vb);
;     const s16x4 c2 = tr_read<v_rd_off(1, 2, 0)>(vb), d2 = tr_read<v_rd_off(1, 2, 1)>(vb), c3 = tr_read<v_rd_off(1, 3, 0)>(vb), d3 = tr_read<v_rd_off(1, 3, 1)>(vb);
;     asm volatile("s_waitcnt lgkmcnt(8)" ::: "memory"); SBAR();
; DEVI void finishSM(f32x16& p0, f32x16& p1, float alpha, float& l_reg, bf16x8& pa0, bf16x8& pa1, bf16x8& pa2, bf16x8& pa3) {
; #pragma unroll
;     for (int r = 0; r < 16; ++r) p1[r] = __builtin_amdgcn_exp2f(p1[r]);
;     f32x2 s2 = (f32x2){p0[0], p0[1]} + (f32x2){p1[0], p1[1]};
; #pragma unroll
;     for (int r = 2; r < 16; r += 2) s2 += (f32x2){p0[r], p0[r + 1]} + (f32x2){p1[r], p1[r + 1]};
;     float ps = s2[0] + s2[1];
;     { auto rr = __builtin_amdgcn_permlane32_swap(__float_as_uint(ps), __float_as_uint(ps), false, false);
;       ps = __uint_as_float(rr[0]) + __uint_as_float(rr[1]); }
;     l_reg = l_reg * alpha + ps;
;     ...
;     PK4(p0, 0, pa0); PK4(p0, 8, pa1); PK4(p1, 0, pa2); PK4(p1, 8, pa3);
;     ...
; }
; DEVI void qkt(f32x16& p0, f32x16& p1, const char* Kb, const bf16x8 (&qr)[6], int r32, int hi, const f32x16& cinit) {
; #pragma unroll
;     for (int d0 = 0; d0 < 6; ++d0) { const int cb = (d0 * 16 + hi * 8) * 2;
;         const bf16x8 k0 = *(const bf16x8*)(Kb + KSWZ(r32, cb)), k1 = *(const bf16x8*)(Kb + KSWZ(32 + r32, cb));
;         p0 = __builtin_amdgcn_mfma_f32_32x32x16_bf16(k0, qr[d0], d0 == 0 ? cinit : p0, 0, 0, 0);
;         p1 = __builtin_amdgcn_mfma_f32_32x32x16_bf16(k1, qr[d0], d0 == 0 ? cinit : p1, 0, 0, 0); }
; }
	v_add_u32_e32 v126, s6, v185
	global_load_lds_dwordx4 v122, s[12:13]
	s_waitcnt lgkmcnt(1)
	v_mfma_f32_32x32x16_bf16 v[98:113], v[210:213], v[138:141], v[98:113]
	s_mov_b32 m0, s99
	v_lshl_add_u64 v[250:251], v[116:117], 0, s[40:41]
	global_load_lds_dwordx4 v[116:117], off
	s_add_i32 m0, s99, 0x2000
	v_add_u32_e32 v174, 0x2000, v202
	global_load_lds_dwordx4 v[250:251], off
	s_waitcnt lgkmcnt(0)
	v_mfma_f32_32x32x16_bf16 v[66:81], v[214:217], v[138:141], v[66:81]
	ds_read_b128 v[210:213], v126
	ds_read_b128 v[214:217], v126 offset:6144
	v_add_u32_e32 v126, s6, v204
	s_waitcnt lgkmcnt(1)
	v_mfma_f32_32x32x16_bf16 v[98:113], v[210:213], v[134:137], v[98:113]
	ds_read_b128 v[210:213], v126
	ds_read_b128 v[218:221], v126 offset:6144
	v_add_u32_e32 v126, s6, v205
	s_waitcnt lgkmcnt(2)
	v_mfma_f32_32x32x16_bf16 v[66:81], v[214:217], v[134:137], v[66:81]
	ds_read_b128 v[214:217], v126
	ds_read_b128 v[222:225], v126 offset:6144
	v_add_u32_e32 v126, s6, v206
	ds_read_b128 v[226:229], v126
	ds_read_b128 v[230:233], v126 offset:6144
	v_add_f32_e32 v126, v50, v82
	v_add_f32_e32 v127, v51, v83
	v_cvt_pk_bf16_f32 v50, v50, v51
	v_cvt_pk_bf16_f32 v51, v52, v53
	s_waitcnt lgkmcnt(5)
	v_mfma_f32_32x32x16_bf16 v[98:113], v[210:213], v[130:133], v[98:113]
	v_add_f32_e64 v210, v52, v84
	v_add_f32_e64 v211, v53, v85
	v_cvt_pk_bf16_f32 v52, v54, v55
	v_cvt_pk_bf16_f32 v53, v56, v57
	v_add_f32_e64 v126, v210, v126
	v_add_f32_e64 v127, v211, v127
	v_add_f32_e64 v210, v54, v86
	v_add_f32_e64 v211, v55, v87
	v_cvt_pk_bf16_f32 v54, v58, v59
	s_waitcnt lgkmcnt(4)
	v_mfma_f32_32x32x16_bf16 v[66:81], v[218:221], v[130:133], v[66:81]
	v_add_f32_e64 v126, v210, v126
	v_add_f32_e64 v127, v211, v127
	v_add_f32_e64 v210, v56, v88
	v_add_f32_e64 v211, v57, v89
	v_cvt_pk_bf16_f32 v55, v60, v61
	v_cvt_pk_bf16_f32 v56, v62, v63
	v_cvt_pk_bf16_f32 v57, v64, v65
	v_add_f32_e64 v126, v210, v126
	v_add_f32_e64 v127, v211, v127
	v_add_f32_e32 v210, v58, v90
	v_add_f32_e32 v211, v59, v91
	v_cvt_pk_bf16_f32 v58, v82, v83
	v_cvt_pk_bf16_f32 v59, v84, v85
	s_waitcnt lgkmcnt(3)
	v_mfma_f32_32x32x16_bf16 v[98:113], v[214:217], v[146:149], v[98:113]
	v_add_f32_e64 v126, v210, v126
	v_add_f32_e64 v127, v211, v127
	v_add_f32_e64 v210, v60, v92
	v_add_f32_e64 v211, v61, v93
	v_cvt_pk_bf16_f32 v60, v86, v87
	v_cvt_pk_bf16_f32 v61, v88, v89
	v_add_f32_e64 v126, v210, v126
	v_add_f32_e64 v127, v211, v127
	v_add_f32_e32 v210, v62, v94
	v_add_f32_e32 v211, v63, v95
	v_cvt_pk_bf16_f32 v62, v90, v91
	v_cvt_pk_bf16_f32 v63, v92, v93
	s_waitcnt lgkmcnt(2)
	v_mfma_f32_32x32x16_bf16 v[66:81], v[222:225], v[146:149], v[66:81]
	v_add_f32_e64 v126, v210, v126
	v_add_f32_e64 v127, v211, v127
	v_add_f32_e64 v210, v64, v96
	v_add_f32_e64 v211, v65, v97
	v_cvt_pk_bf16_f32 v64, v94, v95
	v_cvt_pk_bf16_f32 v65, v96, v97
	ds_read_b64_tr_b16 v[154:155], v174 offset:0
	ds_read_b64_tr_b16 v[156:157], v174 offset:0x400
	ds_read_b64_tr_b16 v[158:159], v174 offset:0x800
	ds_read_b64_tr_b16 v[160:161], v174 offset:0xc00
	ds_read_b64_tr_b16 v[162:163], v174 offset:0x1000
	ds_read_b64_tr_b16 v[164:165], v174 offset:0x1400
	ds_read_b64_tr_b16 v[166:167], v174 offset:0x1800
	ds_read_b64_tr_b16 v[168:169], v174 offset:0x1c00
	v_add_f32_e64 v126, v210, v126
	v_add_f32_e64 v127, v211, v127
	ds_read_b64_tr_b16 v[210:211], v174 offset:0x200
	ds_read_b64_tr_b16 v[212:213], v174 offset:0x600
	ds_read_b64_tr_b16 v[214:215], v174 offset:0xa00
	s_waitcnt lgkmcnt(12)
	v_mfma_f32_32x32x16_bf16 v[98:113], v[226:229], v[142:145], v[98:113]
	ds_read_b64_tr_b16 v[216:217], v174 offset:0xe00
	ds_read_b64_tr_b16 v[218:219], v174 offset:0x1200
	ds_read_b64_tr_b16 v[220:221], v174 offset:0x1600
	ds_read_b64_tr_b16 v[222:223], v174 offset:0x1a00
	ds_read_b64_tr_b16 v[224:225], v174 offset:0x1e00
	v_add_f32_e32 v126, v126, v127
	s_waitcnt lgkmcnt(15)
	v_mfma_f32_32x32x16_bf16 v[66:81], v[230:233], v[142:145], v[66:81]
	v_mov_b32_e32 v127, v126


; DEVI void pv_both(f32x16& o0, f32x16& o1, int vb, bf16x8 pa0, bf16x8 pa1, bf16x8 pa2, bf16x8 pa3) {
;     const s16x4 a0 = tr_read<v_rd_off(0, 0, 0)>(vb), b0 = tr_read<v_rd_off(0, 0, 1)>(vb), a1 = tr_read<v_rd_off(0, 1, 0)>(vb), b1 = tr_read<v_rd_off(0, 1, 1)>(vb);
;     const s16x4 a2 = tr_read<v_rd_off(0, 2, 0)>(vb), b2 = tr_read<v_rd_off(0, 2, 1)>(vb), a3 = tr_read<v_rd_off(0, 3, 0)>(vb), b3 = tr_read<v_rd_off(0, 3, 1)>(vb);
;     const s16x4 c0 = tr_read<v_rd_off(1, 0, 0)>(vb), d0 = tr_read<v_rd_off(1, 0, 1)>(vb), c1 = tr_read<v_rd_off(1, 1, 0)>(vb), d1 = tr_read<v_rd_off(1, 1, 1)>(vb);
;     const s16x4 c2 = tr_read<v_rd_off(1, 2, 0)>(vb), d2 = tr_read<v_rd_off(1, 2, 1)>(vb), c3 = tr_read<v_rd_off(1, 3, 0)>(vb), d3 = tr_read<v_rd_off(1, 3, 1)>(vb);
;     asm volatile("s_waitcnt lgkmcnt(8)" ::: "memory"); SBAR();
;     ...
;     o0 = __builtin_amdgcn_mfma_f32_32x32x16_bf16(pa0, PK(a0, b0), o0, 0, 0, 0);
;     o0 = __builtin_amdgcn_mfma_f32_32x32x16_bf16(pa1, PK(a1, b1), o0, 0, 0, 0);
;     o0 = __builtin_amdgcn_mfma_f32_32x32x16_bf16(pa2, PK(a2, b2), o0, 0, 0, 0);
;     o0 = __builtin_amdgcn_mfma_f32_32x32x16_bf16(pa3, PK(a3, b3), o0, 0, 0, 0);
;     asm volatile("s_waitcnt lgkmcnt(0)" ::: "memory"); SBAR();
;     o1 = __builtin_amdgcn_mfma_f32_32x32x16_bf16(pa0, PK(c0, d0), o1, 0, 0, 0);
;     o1 = __builtin_amdgcn_mfma_f32_32x32x16_bf16(pa1, PK(c1, d1), o1, 0, 0, 0);
;     o1 = __builtin_amdgcn_mfma_f32_32x32x16_bf16(pa2, PK(c2, d2), o1, 0, 0, 0);
;     o1 = __builtin_amdgcn_mfma_f32_32x32x16_bf16(pa3, PK(c3, d3), o1, 0, 0, 0);
;     ...
; }
; template <bool FIRST> DEVI bool partialSM(f32x16& p0, f32x16& p1, float& m_reg, float& alpha) {
;     float pmax = p0[0];
; #pragma unroll
;     for (int r = 1; r < 16; ++r) pmax = fmaxf(pmax, p0[r]);
; #pragma unroll
;     for (int r = 0; r < 16; ++r) pmax = fmaxf(pmax, p1[r]);
;     { auto rr = __builtin_amdgcn_permlane32_swap(__float_as_uint(pmax), __float_as_uint(pmax), false, false);
;       pmax = fmaxf(__uint_as_float(rr[0]), __uint_as_float(rr[1])); }
;     if (FIRST) { m_reg = pmax; alpha = 1.f;
; #pragma unroll
;         for (int r = 0; r < 16; ++r) { p0[r] = __builtin_amdgcn_exp2f(p0[r] - pmax); p1[r] = p1[r] - pmax; }
;         return false;
;     } else if (__builtin_expect(__all(pmax <= ATT_THR), 1)) { alpha = 1.f;
; #pragma unroll
;         for (int r = 0; r < 16; ++r) p0[r] = __builtin_amdgcn_exp2f(p0[r]);
	s_waitcnt lgkmcnt(14)
	v_mfma_f32_32x32x16_bf16 v[18:33], v[50:53], v[154:157], v[18:33]
	v_permlane32_swap_b32_e32 v126, v127
	s_waitcnt lgkmcnt(6)
	v_mfma_f32_32x32x16_bf16 v[2:17], v[50:53], v[210:213], v[2:17]
	s_nop 1
	v_max_f32_e32 v249, v99, v99
	v_max_f32_e32 v250, v98, v98
	v_max_f32_e32 v249, v250, v249
	v_max3_f32 v249, v249, v100, v101
	v_max3_f32 v249, v249, v102, v103
	v_max3_f32 v251, v249, v104, v105
	v_max3_f32 v251, v251, v106, v107
	v_exp_f32_e32 v50, v98
	v_exp_f32_e32 v51, v99
	v_exp_f32_e32 v52, v100
	v_exp_f32_e32 v53, v101
	v_mfma_f32_32x32x16_bf16 v[18:33], v[54:57], v[158:161], v[18:33]
	s_waitcnt lgkmcnt(4)
	v_mfma_f32_32x32x16_bf16 v[2:17], v[54:57], v[214:217], v[2:17]
	v_max3_f32 v251, v251, v108, v109
	v_max3_f32 v251, v251, v110, v111
	v_max3_f32 v251, v251, v112, v113
	v_max3_f32 v251, v251, v66, v67
	v_max3_f32 v251, v251, v68, v69
	v_max3_f32 v251, v251, v70, v71
	v_max3_f32 v251, v251, v72, v73
	v_exp_f32_e32 v54, v102
	v_exp_f32_e32 v55, v103
	v_exp_f32_e32 v56, v104
	v_exp_f32_e32 v57, v105
	v_mfma_f32_32x32x16_bf16 v[18:33], v[58:61], v[162:165], v[18:33]
	s_waitcnt lgkmcnt(2)
	v_mfma_f32_32x32x16_bf16 v[2:17], v[58:61], v[218:221], v[2:17]
	v_max3_f32 v251, v251, v74, v75
	v_max3_f32 v251, v251, v76, v77
	v_max3_f32 v251, v251, v78, v79
	v_max3_f32 v251, v251, v80, v81
	v_mov_b32_e32 v252, v251


; #define SBAR() __builtin_amdgcn_sched_barrier(0)
; DEVI void pv_both(f32x16& o0, f32x16& o1, int vb, bf16x8 pa0, bf16x8 pa1, bf16x8 pa2, bf16x8 pa3) {
;     ...
;     o0 = __builtin_amdgcn_mfma_f32_32x32x16_bf16(pa0, PK(a0, b0), o0, 0, 0, 0);
;     o0 = __builtin_amdgcn_mfma_f32_32x32x16_bf16(pa1, PK(a1, b1), o0, 0, 0, 0);
;     o0 = __builtin_amdgcn_mfma_f32_32x32x16_bf16(pa2, PK(a2, b2), o0, 0, 0, 0);
;     o0 = __builtin_amdgcn_mfma_f32_32x32x16_bf16(pa3, PK(a3, b3), o0, 0, 0, 0);
;     asm volatile("s_waitcnt lgkmcnt(0)" ::: "memory"); SBAR();
;     o1 = __builtin_amdgcn_mfma_f32_32x32x16_bf16(pa0, PK(c0, d0), o1, 0, 0, 0);
;     o1 = __builtin_amdgcn_mfma_f32_32x32x16_bf16(pa1, PK(c1, d1), o1, 0, 0, 0);
;     o1 = __builtin_amdgcn_mfma_f32_32x32x16_bf16(pa2, PK(c2, d2), o1, 0, 0, 0);
;     o1 = __builtin_amdgcn_mfma_f32_32x32x16_bf16(pa3, PK(c3, d3), o1, 0, 0, 0);
; template <bool FIRST> DEVI bool partialSM(f32x16& p0, f32x16& p1, float& m_reg, float& alpha) {
;     float pmax = p0[0];
; #pragma unroll
;     for (int r = 1; r < 16; ++r) pmax = fmaxf(pmax, p0[r]);
; #pragma unroll
;     for (int r = 0; r < 16; ++r) pmax = fmaxf(pmax, p1[r]);
;     { auto rr = __builtin_amdgcn_permlane32_swap(__float_as_uint(pmax), __float_as_uint(pmax), false, false);
;       pmax = fmaxf(__uint_as_float(rr[0]), __uint_as_float(rr[1])); }
;     if (FIRST) { m_reg = pmax; alpha = 1.f;
; #pragma unroll
;         for (int r = 0; r < 16; ++r) { p0[r] = __builtin_amdgcn_exp2f(p0[r] - pmax); p1[r] = p1[r] - pmax; }
;         return false;
;     } else if (__builtin_expect(__all(pmax <= ATT_THR), 1)) { alpha = 1.f;
; #pragma unroll
;         for (int r = 0; r < 16; ++r) p0[r] = __builtin_amdgcn_exp2f(p0[r]);
	v_exp_f32_e32 v58, v106
	v_exp_f32_e32 v59, v107
	v_permlane32_swap_b32_e32 v251, v252
	v_exp_f32_e32 v60, v108
	v_exp_f32_e32 v61, v109
	v_mfma_f32_32x32x16_bf16 v[18:33], v[62:65], v[166:169], v[18:33]
	s_waitcnt lgkmcnt(0)
	v_mfma_f32_32x32x16_bf16 v[2:17], v[62:65], v[222:225], v[2:17]
	v_exp_f32_e32 v62, v110
	v_exp_f32_e32 v63, v111
	v_exp_f32_e32 v64, v112
	v_exp_f32_e32 v65, v113
	v_max_f32_e32 v252, v252, v252
	v_max_f32_e32 v251, v251, v251
	v_max_f32_e32 v174, v251, v252
	v_cmp_ge_f32_e32 vcc, s79, v174
	s_cmp_lg_u64 vcc, exec
	s_cselect_b64 s[6:7], -1, 0
	s_cbranch_scc1 .LBB0_711
	v_mov_b32_e32 v202, 1.0
	v_mov_b32_e32 v203, v209
	s_branch .LBB0_716

; #define VM0() asm volatile("s_waitcnt vmcnt(0)" ::: "memory")
; #define B_RESC(a, rare) do { if (rare) { if (hi == 0) al_l[r32] = (a); asm volatile("s_waitcnt lgkmcnt(0)" ::: "memory"); __builtin_amdgcn_wave_barrier(); \
;         _Pragma("unroll") for (int _d = 0; _d < 2; ++_d) _Pragma("unroll") for (int _r = 0; _r < 16; ++_r) o[_d][_r] *= al_l[crow(_r, hi)]; C_SPLAT(); } } while (0)
; DEVI void attn_unit8(const Params& p, char* smem, int unit, int l, int& cvs  , CvRun& crun) {
;     ...
;     for (int T = 0; T + 1 < NTILE; ++T) {
;         const char* Kb = K_lds + s0 * 24576; const int vb = vb0 + s0 * 16384;
;         CvRegs cvr; cv_issue(p, l, cvs, lane, cvr, crun); cvs += (int)gridDim.x * 8;
;         qkt(pB0, pB1, Kb + 12288, qr, r32, hi, cinit);
;         finishSM(pA0, pA1, alA, l_reg, pa0, pa1, pa2, pa3);
;         pv_both(o[0], o[1], vb, pa0, pa1, pa2, pa3);
;         { const bool rr_ = partialSM<false>(pB0, pB1, m_reg, alB); B_RESC(alB, rr_); }
;         cv_finish(smem + 124928 + wid * 2304, lane, cvr);
;         if (cvr.live) asm volatile("s_waitcnt vmcnt(2)" ::: "memory"); else VM0();
;         __syncthreads();
;         if (T + 2 < NTILE) B_DMA(T + 2, s2);
;         qkt(pA0, pA1, K_lds + s1 * 24576, qr, r32, hi, cinit);
;         finishSM(pB0, pB1, alB, l_reg, pa0, pa1, pa2, pa3);
;         pv_both(o[0], o[1], vb + 8192, pa0, pa1, pa2, pa3);
;         { const bool rr_ = partialSM<false>(pA0, pA1, m_reg, alA); B_RESC(alA, rr_); }
;         { const int t = s0; s0 = s1; s1 = s2; s2 = t; }
;     }
.LBB0_716:
	s_add_i32 s54, s54, s86
	v_add_f32_e32 v82, v124, v125
	s_add_u32 s12, s12, 0x6000
	v_fmac_f32_e32 v82, v188, v207
	v_add_f32_e32 v188, v126, v127
	s_addc_u32 s13, s13, 0
	v_fmac_f32_e32 v188, v82, v208
	s_cmp_eq_u32 s12, s67
	v_lshl_add_u64 v[116:117], v[116:117], 0, s[44:45]
	s_cbranch_scc1 .LBB0_718
	s_mov_b32 s6, s89
	s_mov_b32 s89, s61
	v_mov_b32_e32 v207, v202
	s_branch .LBB0_666

; DEVI int tidx() { int t = threadIdx.x; asm volatile("" : "+v"(t)); __builtin_assume(t >= 0 && t < 512); return t; }
; DEVI unsigned cvt_pk_bf16(float lo, float hi) { unsigned r; asm volatile("v_cvt_pk_bf16_f32 %0, %1, %2" : "=v"(r) : "v"(lo), "v"(hi)); return r; }
; DEVI float bf2f(bf16_t h) { return __uint_as_float(((unsigned)h) << 16); }
; DEVI void attn_unit8(const Params& p, char* smem, int unit, int l, int& cvs  , CvRun& crun) {
;     const int tid = tidx(), wid = __builtin_amdgcn_readfirstlane(tid >> 6), lane = tid & 63, r32 = lane & 31, hi = lane >> 5;
;     const int x8 = unit & 7, v8 = unit >> 3, bh = x8 + 8 * (v8 >> 4), qt = v8 & 15, b = bh >> 3, hh = bh & 7;
;     char* K_lds = smem; char* V_lds = smem + 73728;
;     float* wsx = (float*)(smem + 122880) + wid * 64; float* li_l = wsx; float* al_l = wsx + 32;
;     const bf16_t* Kg = p.kfull + (size_t)bh * S_ * 96; const bf16_t* Vg = p.vfull + (size_t)bh * S_ * 64;
;     const size_t qtok = (size_t)b * S_ + qt * 256 + wid * 32 + r32;
;     bf16x8 qr[6];
;     { const bf16_t* qp = p.qbuf + qtok * 768 + hh * 96 + hi * 8;
; #pragma unroll
;       for (int d0 = 0; d0 < 6; ++d0) qr[d0] = *(const bf16x8*)(qp + d0 * 16);
;       const f32x4 c0 = *(const f32x4*)(p.cs + qtok * 16 + hi * 8), c1 = *(const f32x4*)(p.cs + qtok * 16 + hi * 8 + 4);
;       const f32x4 s0 = *(const f32x4*)(p.sn + qtok * 16 + hi * 8), s1 = *(const f32x4*)(p.sn + qtok * 16 + hi * 8 + 4);
;       float o1[8], o2[8];
; #pragma unroll
;       for (int j = 0; j < 8; ++j) { const float x1 = bf2f((bf16_t)qr[4][j]), x2 = bf2f((bf16_t)qr[5][j]); const float cc = j < 4 ? c0[j] : c1[j - 4], ss = j < 4 ? s0[j] : s1[j - 4];
;           o1[j] = x1 * cc - x2 * ss; o2[j] = x2 * cc + x1 * ss; }
;       u32x4 w1, w2;
; #pragma unroll
;       for (int j = 0; j < 4; ++j) { w1[j] = cvt_pk_bf16(o1[2 * j], o1[2 * j + 1]); w2[j] = cvt_pk_bf16(o2[2 * j], o2[2 * j + 1]); }
;       qr[4] = *(bf16x8*)&w1; qr[5] = *(bf16x8*)&w2; }
.LBB0_2229:
	v_mov_b32_e32 v86, v0
	s_ashr_i32 s5, s87, 4
	v_readfirstlane_b32 s4, v86
	s_lshr_b32 s53, s4, 6
	s_and_b32 s52, s5, -8
	s_and_b32 s8, s4, 0x3fffffc0
	s_load_dwordx4 s[4:7], s[24:25], 0x1a0
	s_load_dwordx4 s[12:15], s[24:25], 0x110
	s_and_b32 s92, s87, 7
	s_ashr_i32 s16, s87, 7
	s_lshl_b32 s8, s8, 2
	s_or_b32 s10, s52, s92
	s_add_i32 s93, s8, 0
	s_ashr_i32 s17, s16, 31
	s_lshl_b32 s8, s87, 5
	s_ashr_i32 s11, s10, 31
	s_lshl_b64 s[16:17], s[16:17], 12
	s_and_b32 s8, s8, 0xf00
	s_and_b32 s2, s62, 7
	s_add_i32 s93, s93, 0x1e000
	s_waitcnt lgkmcnt(0)
	v_mov_b32_e32 v2, s4
	v_mov_b32_e32 v3, s5
	s_lshl_b64 s[4:5], s[10:11], 19
	s_or_b32 s8, s16, s8
	s_lshl_b32 s11, s53, 5
	v_and_b32_e32 v176, 31, v86
	s_add_u32 s48, s8, s11
	v_or_b32_e32 v10, s48, v176
	s_addc_u32 s49, s17, 0
	v_mad_u64_u32 v[2:3], s[16:17], v10, s74, v[2:3]
	v_bfe_u32 v187, v86, 5, 1
	v_mad_i32_i24 v3, s49, v181, v3
	s_mul_i32 s8, s92, 0xc0
	v_mov_b32_e32 v11, s49
	v_lshl_add_u64 v[2:3], v[2:3], 0, s[8:9]
	v_lshlrev_b32_e32 v178, 4, v187
	v_mov_b32_e32 v179, v175
	v_lshl_add_u64 v[26:27], v[2:3], 0, v[178:179]
	v_lshlrev_b64 v[10:11], 6, v[10:11]
	global_load_dwordx4 v[2:5], v[26:27], off offset:128
	global_load_dwordx4 v[6:9], v[26:27], off offset:160
	v_lshl_add_u64 v[12:13], s[12:13], 0, v[10:11]
	v_and_b32_e32 v174, 32, v86
	v_lshl_add_u64 v[10:11], s[14:15], 0, v[10:11]
	v_lshl_add_u64 v[22:23], v[12:13], 0, v[174:175]
	v_lshl_add_u64 v[18:19], v[10:11], 0, v[174:175]
	global_load_dwordx4 v[10:13], v[18:19], off
	global_load_dwordx4 v[14:17], v[22:23], off
	s_nop 0
	global_load_dwordx4 v[18:21], v[18:19], off offset:16
	s_nop 0
	global_load_dwordx4 v[22:25], v[22:23], off offset:16
	s_load_dwordx2 s[50:51], s[24:25], 0x1b0
	global_load_dwordx4 v[150:153], v[26:27], off
	global_load_dwordx4 v[138:141], v[26:27], off offset:32
	global_load_dwordx4 v[134:137], v[26:27], off offset:64
	global_load_dwordx4 v[130:133], v[26:27], off offset:96
	s_mul_hi_i32 s8, s10, 0xc0000
	s_mul_i32 s10, s10, 0xc0000
	s_add_u32 s10, s6, s10
	s_addc_u32 s11, s7, s8
	s_lshl_b32 s61, s53, 10
	s_add_i32 s96, s61, 0
	s_waitcnt lgkmcnt(0)
	s_add_u32 s4, s50, s4
	s_mov_b32 m0, s96
	v_lshlrev_b32_e32 v88, 6, v187
	s_addc_u32 s5, s51, s5
	s_add_i32 s97, s76, s61
	v_lshlrev_b32_e32 v90, 2, v86
	v_and_b32_e32 v91, 63, v86
	v_lshlrev_b32_e32 v93, 4, v91
	v_lshlrev_b32_e32 v92, 3, v91
	v_lshlrev_b32_e32 v94, 1, v91
	s_mov_b32 s8, s9
	s_mov_b32 s12, s9
	s_mov_b32 s13, s9
	s_mov_b32 s14, s9
	s_mov_b32 s15, s9
	s_mov_b32 s16, s9
	s_mov_b32 s17, s9
	s_mov_b32 s18, s9
	s_mov_b32 s19, s9
	s_mov_b32 s20, s9
	s_mov_b32 s21, s9
	s_mov_b32 s22, s9
	s_mov_b32 s23, s9
	s_mulk_i32 s53, 0x900
	v_mov_b32_e32 v83, v175
	v_mov_b32_e32 v85, v175
	v_and_b32_e32 v114, 28, v90
	v_lshl_add_u32 v188, v176, 2, s93
	v_mul_u32_u24_e32 v202, 0x44, v114
	v_bfe_u32 v196, v91, 1, 2
	v_mov_b32_e32 v208, 1.0
	s_mov_b32 s71, s9
	v_mov_b32_e32 v189, v175
	s_waitcnt vmcnt(9)
	v_lshlrev_b32_e32 v27, 16, v2
	s_waitcnt vmcnt(8)
	v_lshlrev_b32_e32 v26, 16, v6
	v_and_b32_e32 v33, 0xffff0000, v2
	v_lshlrev_b32_e32 v35, 16, v3
	s_waitcnt vmcnt(7)
	v_mov_b32_e32 v28, v10
	s_waitcnt vmcnt(6)
	v_mov_b32_e32 v29, v14
	v_mov_b32_e32 v36, v12
	v_mov_b32_e32 v37, v16
	v_mov_b32_e32 v38, v16
	v_mov_b32_e32 v39, v12
	v_and_b32_e32 v3, 0xffff0000, v3
	v_and_b32_e32 v2, 0xffff0000, v7
	v_mov_b32_e32 v16, v13
	v_mov_b32_e32 v12, v17
	v_and_b32_e32 v32, 0xffff0000, v6
	v_lshlrev_b32_e32 v34, 16, v7
	v_pk_mul_f32 v[6:7], v[28:29], v[26:27]
	v_pk_mul_f32 v[16:17], v[16:17], v[2:3]
	v_pk_mul_f32 v[2:3], v[12:13], v[2:3]
	v_mov_b32_e32 v30, v14
	v_mov_b32_e32 v31, v10
	v_sub_f32_e32 v12, v7, v6
	v_sub_f32_e32 v16, v17, v16
	v_add_f32_e32 v17, v2, v3
	v_lshlrev_b32_e32 v3, 16, v4
	v_lshlrev_b32_e32 v2, 16, v8
	s_waitcnt vmcnt(5)
	v_mov_b32_e32 v6, v18
	s_waitcnt vmcnt(4)
	v_mov_b32_e32 v7, v22
	v_pk_mul_f32 v[26:27], v[30:31], v[26:27]
	v_pk_mul_f32 v[6:7], v[6:7], v[2:3]
	v_add_f32_e32 v13, v26, v27
	v_sub_f32_e32 v26, v7, v6
	v_mov_b32_e32 v6, v22
	v_mov_b32_e32 v7, v18
	v_pk_mul_f32 v[2:3], v[6:7], v[2:3]
	v_mov_b32_e32 v22, v19
	v_add_f32_e32 v27, v2, v3
	v_and_b32_e32 v3, 0xffff0000, v4
	v_and_b32_e32 v2, 0xffff0000, v8
	v_mov_b32_e32 v18, v23
	v_pk_mul_f32 v[6:7], v[22:23], v[2:3]
	v_pk_mul_f32 v[2:3], v[18:19], v[2:3]
	v_sub_f32_e32 v8, v7, v6
	v_add_f32_e32 v18, v2, v3
	v_lshlrev_b32_e32 v3, 16, v5
	v_lshlrev_b32_e32 v2, 16, v9
	v_mov_b32_e32 v6, v20
	v_mov_b32_e32 v7, v24
	v_pk_mul_f32 v[6:7], v[6:7], v[2:3]
	v_mov_b32_e32 v14, v11
	v_sub_f32_e32 v19, v7, v6
	v_mov_b32_e32 v6, v24
	v_mov_b32_e32 v7, v20
	v_pk_mul_f32 v[2:3], v[6:7], v[2:3]
	v_mov_b32_e32 v24, v21
	v_add_f32_e32 v6, v2, v3
	v_and_b32_e32 v3, 0xffff0000, v5
	v_and_b32_e32 v2, 0xffff0000, v9
	v_mov_b32_e32 v20, v25
	v_mov_b32_e32 v10, v15
	v_pk_mul_f32 v[4:5], v[24:25], v[2:3]
	v_pk_mul_f32 v[2:3], v[20:21], v[2:3]
	v_pk_mul_f32 v[14:15], v[14:15], v[32:33]
	v_pk_mul_f32 v[10:11], v[10:11], v[32:33]
	v_pk_mul_f32 v[28:29], v[36:37], v[34:35]
	v_pk_mul_f32 v[30:31], v[38:39], v[34:35]
	v_add_f32_e32 v2, v2, v3
	v_sub_f32_e32 v14, v15, v14
	v_add_f32_e32 v10, v10, v11
	v_sub_f32_e32 v11, v29, v28
	v_add_f32_e32 v15, v30, v31
	v_sub_f32_e32 v4, v5, v4
	v_cvt_pk_bf16_f32 v146, v12, v14
	v_cvt_pk_bf16_f32 v142, v13, v10
	v_cvt_pk_bf16_f32 v147, v11, v16
	v_cvt_pk_bf16_f32 v143, v15, v17
	v_cvt_pk_bf16_f32 v148, v26, v8
	v_cvt_pk_bf16_f32 v144, v27, v18
	v_cvt_pk_bf16_f32 v149, v19, v4
	v_cvt_pk_bf16_f32 v145, v6, v2
	v_mul_u32_u24_e32 v2, 0xaaab, v86
	v_lshrrev_b32_e32 v3, 19, v2
	v_mul_lo_u16_e32 v4, 12, v3
	v_sub_u16_e32 v4, v86, v4
	v_lshrrev_b32_e32 v2, 21, v2
; #define LAS __attribute__((address_space(3)))
; DEVI int v_rd_base(int lane) { return ((lane & 3) << 3) | (((lane >> 2) & 3) << 6) | (((lane >> 4) & 1) << 5) | (((lane >> 5) & 1) << 8); }
; #define VM0() asm volatile("s_waitcnt vmcnt(0)" ::: "memory")
; DEVI void attn_unit8(const Params& p, char* smem, int unit, int l, int& cvs  , CvRun& crun) {
;     ...
;     int ksrc[3];
; #pragma unroll
;     for (int i = 0; i < 3; ++i) { const int pc = tid + 512 * i, row = pc / 12, ch = (pc % 12) ^ ((row >> 2) & 3); ksrc[i] = row * 192 + ch * 16; }
;     const int vsrc = wid * 1024 + ((lane >> 2) & 7) * 128 + (lane >> 5) * 64 + (lane & 3) * 16;
;     LAS char* const Kl = (LAS char*)K_lds + wid * 1024; LAS char* const Vl = (LAS char*)V_lds + wid * 1024;
;     ...
;     const int vb0 = (int)(uintptr_t)(LAS char*)V_lds + v_rd_base(lane);
;     float m_reg = 0.f, l_reg = 0.f; f32x16 o[2];
; #pragma unroll
;     for (int d = 0; d < 2; ++d)
; #pragma unroll
;         for (int r = 0; r < 16; ++r) o[d][r] = 0.f;
;     f32x16 pA0, pA1, pB0, pB1; float alA, alB; bf16x8 pa0, pa1, pa2, pa3;
;     constexpr int NTILE = S_ / 128;
;     B_DMA(0, 0); B_DMA(1, 1); VM0(); __syncthreads();
	v_bitop3_b32 v2, v2, v4, 3 bitop3:0x6c
	v_mul_u32_u24_e32 v3, 0xc0, v3
	v_lshl_add_u32 v174, v2, 4, v3
	v_or_b32_e32 v2, 0x200, v86
	v_mul_u32_u24_sdwa v3, v2, s75 dst_sel:DWORD dst_unused:UNUSED_PAD src0_sel:WORD_0 src1_sel:DWORD
	v_lshrrev_b32_e32 v4, 19, v3
	v_mul_lo_u16_e32 v5, 12, v4
	v_sub_u16_e32 v2, v2, v5
	v_lshrrev_b32_e32 v3, 21, v3
	v_bitop3_b32 v2, v3, v2, 3 bitop3:0x6c
	v_mul_u32_u24_e32 v3, 0xc0, v4
	v_lshl_add_u32 v82, v2, 4, v3
	v_or_b32_e32 v2, 0x400, v86
	v_mul_u32_u24_sdwa v3, v2, s75 dst_sel:DWORD dst_unused:UNUSED_PAD src0_sel:WORD_0 src1_sel:DWORD
	v_lshrrev_b32_e32 v4, 19, v3
	v_mul_lo_u16_e32 v5, 12, v4
	v_sub_u16_e32 v2, v2, v5
	v_lshrrev_b32_e32 v3, 21, v3
	v_bitop3_b32 v2, v3, v2, 3 bitop3:0x6c
	v_mul_u32_u24_e32 v3, 0xc0, v4
	v_lshl_add_u32 v84, v2, 4, v3
	v_lshlrev_b32_e32 v2, 5, v86
	v_and_b32_e32 v87, 0x380, v2
	v_lshlrev_b32_e32 v3, 4, v86
	global_load_lds_dwordx4 v174, s[10:11]
	s_add_i32 m0, s96, 0x2000
	v_or_b32_e32 v2, v88, v87
	v_and_b32_e32 v89, 48, v3
	global_load_lds_dwordx4 v82, s[10:11]
	s_add_i32 m0, s96, 0x4000
	v_or3_b32 v2, v2, v89, s61
	global_load_lds_dwordx4 v84, s[10:11]
	v_mov_b32_e32 v3, v175
	s_mov_b32 m0, s97
	v_lshl_add_u64 v[4:5], s[4:5], 0, v[2:3]
	global_load_lds_dwordx4 v2, s[4:5]
	s_add_i32 m0, s97, 0x2000
	v_lshl_add_u64 v[2:3], v[4:5], 0, s[40:41]
	s_add_u32 s4, s10, 0x6000
	global_load_lds_dwordx4 v[2:3], off
	s_addc_u32 s5, s11, 0
	s_add_i32 m0, s96, 0x6000
	v_lshl_add_u64 v[2:3], v[4:5], 0, s[44:45]
	global_load_lds_dwordx4 v174, s[4:5]
	s_add_i32 m0, s96, 0x8000
	v_mul_u32_u24_e32 v10, 0xc0, v176
	global_load_lds_dwordx4 v82, s[4:5]
	s_add_i32 m0, s96, 0xa000
	v_and_b32_e32 v11, 48, v90
	global_load_lds_dwordx4 v84, s[4:5]
	s_add_i32 m0, s97, 0x4000
	v_bitop3_b32 v129, v178, v10, v11 bitop3:0xde
	global_load_lds_dwordx4 v[2:3], off
	v_lshl_add_u64 v[2:3], v[4:5], 0, s[42:43]
	s_add_i32 m0, s97, 0x6000
	v_add_u32_e32 v190, 0, v129
	global_load_lds_dwordx4 v[2:3], off
	s_waitcnt vmcnt(0)
	s_waitcnt vmcnt(0) lgkmcnt(0)
	s_barrier
; #define VM0() asm volatile("s_waitcnt vmcnt(0)" ::: "memory")
; #define C_SPLAT() do { _Pragma("unroll") for (int _r = 0; _r < 16; ++_r) cinit[_r] = -m_reg; asm volatile("" : "+v"(cinit)); } while (0)
; template <bool FIRST> DEVI bool partialSM(f32x16& p0, f32x16& p1, float& m_reg, float& alpha) {
;     float pmax = p0[0];
; #pragma unroll
;     for (int r = 1; r < 16; ++r) pmax = fmaxf(pmax, p0[r]);
; #pragma unroll
;     for (int r = 0; r < 16; ++r) pmax = fmaxf(pmax, p1[r]);
;     { auto rr = __builtin_amdgcn_permlane32_swap(__float_as_uint(pmax), __float_as_uint(pmax), false, false);
;       pmax = fmaxf(__uint_as_float(rr[0]), __uint_as_float(rr[1])); }
;     if (FIRST) { m_reg = pmax; alpha = 1.f;
; #pragma unroll
;         for (int r = 0; r < 16; ++r) { p0[r] = __builtin_amdgcn_exp2f(p0[r] - pmax); p1[r] = p1[r] - pmax; }
;         return false;
; DEVI void attn_unit8(const Params& p, char* smem, int unit, int l, int& cvs  , CvRun& crun) {
;     ...
;     float m_reg = 0.f, l_reg = 0.f; f32x16 o[2];
; #pragma unroll
;     for (int d = 0; d < 2; ++d)
; #pragma unroll
;         for (int r = 0; r < 16; ++r) o[d][r] = 0.f;
;     f32x16 pA0, pA1, pB0, pB1; float alA, alB; bf16x8 pa0, pa1, pa2, pa3;
;     constexpr int NTILE = S_ / 128;
;     B_DMA(0, 0); B_DMA(1, 1); VM0(); __syncthreads();
;     f32x16 cinit;
;     ...
;     { f32x16 z; _Pragma("unroll") for (int r = 0; r < 16; ++r) z[r] = 0.f;
;       qkt(pA0, pA1, K_lds, qr, r32, hi, z); } partialSM<true>(pA0, pA1, m_reg, alA); C_SPLAT();
;     int s0 = 0, s1 = 1, s2 = 2;
	ds_read_b128 v[2:5], v190
	ds_read_b128 v[6:9], v190 offset:6144
	s_waitcnt lgkmcnt(1)
	v_mfma_f32_32x32x16_bf16 v[34:49], v[2:5], v[150:153], 0
	v_or_b32_e32 v2, 32, v178
	v_bitop3_b32 v184, v2, v10, v11 bitop3:0xde
	v_add_u32_e32 v191, 0, v184
	s_mov_b32 s10, s9
	s_mov_b32 s11, s9
	s_lshl_b32 s84, s54, 5
	s_lshl_b32 s85, s54, 4
	s_waitcnt lgkmcnt(0)
	v_mfma_f32_32x32x16_bf16 v[18:33], v[6:9], v[150:153], 0
	ds_read_b128 v[2:5], v191
	ds_read_b128 v[6:9], v191 offset:6144
	s_lshl_b32 s88, s54, 3
	s_lshl_b32 s70, s54, 1
	v_cmp_gt_u32_e64 s[4:5], 32, v91
	s_waitcnt lgkmcnt(1)
	v_mfma_f32_32x32x16_bf16 v[34:49], v[2:5], v[138:141], v[34:49]
	v_or_b32_e32 v2, 64, v178
	v_xad_u32 v185, v2, v11, v10
	v_add_u32_e32 v192, 0, v185
	s_waitcnt lgkmcnt(0)
	v_mfma_f32_32x32x16_bf16 v[18:33], v[6:9], v[138:141], v[18:33]
	ds_read_b128 v[2:5], v192
	ds_read_b128 v[6:9], v192 offset:6144
	s_waitcnt lgkmcnt(1)
	v_mfma_f32_32x32x16_bf16 v[34:49], v[2:5], v[134:137], v[34:49]
	v_or_b32_e32 v2, 0x60, v178
	v_xad_u32 v205, v2, v11, v10
	v_add_u32_e32 v193, 0, v205
	ds_read_b128 v[2:5], v193
	s_waitcnt lgkmcnt(1)
	v_mfma_f32_32x32x16_bf16 v[18:33], v[6:9], v[134:137], v[18:33]
	ds_read_b128 v[6:9], v193 offset:6144
	s_waitcnt lgkmcnt(1)
	v_mfma_f32_32x32x16_bf16 v[34:49], v[2:5], v[130:133], v[34:49]
	v_and_b32_e32 v2, 0xc0, v93
	v_and_or_b32 v12, v92, 24, v2
	v_or_b32_e32 v2, 0x80, v178
	v_xad_u32 v206, v2, v11, v10
	v_add_u32_e32 v194, 0, v206
	ds_read_b128 v[2:5], v194
	s_waitcnt lgkmcnt(1)
	v_mfma_f32_32x32x16_bf16 v[18:33], v[6:9], v[130:133], v[18:33]
	v_and_b32_e32 v6, 32, v94
	v_and_b32_e32 v7, 0x100, v92
	v_or3_b32 v179, v12, v6, v7
	ds_read_b128 v[6:9], v194 offset:6144
	v_add_u32_e32 v115, s76, v179
	s_waitcnt lgkmcnt(1)
	v_mfma_f32_32x32x16_bf16 v[34:49], v[2:5], v[146:149], v[34:49]
	v_or_b32_e32 v2, 0xa0, v178
	v_xad_u32 v207, v2, v11, v10
	v_add_u32_e32 v195, 0, v207
	ds_read_b128 v[2:5], v195
	ds_read_b128 v[50:53], v195 offset:6144
	s_waitcnt lgkmcnt(2)
	v_mfma_f32_32x32x16_bf16 v[18:33], v[6:9], v[146:149], v[18:33]
	s_waitcnt lgkmcnt(1)
	v_mfma_f32_32x32x16_bf16 v[34:49], v[2:5], v[142:145], v[34:49]
	v_mov_b64_e32 v[2:3], s[8:9]
	v_mov_b64_e32 v[4:5], s[10:11]
	v_mov_b64_e32 v[6:7], s[12:13]
	v_mov_b64_e32 v[8:9], s[14:15]
	v_mov_b64_e32 v[10:11], s[16:17]
	v_mov_b64_e32 v[12:13], s[18:19]
	v_mov_b64_e32 v[14:15], s[20:21]
	s_waitcnt lgkmcnt(0)
	v_mfma_f32_32x32x16_bf16 v[18:33], v[50:53], v[142:145], v[18:33]
	s_nop 2
	v_max_f32_e32 v50, v35, v35
	v_max_f32_e32 v51, v34, v34
	v_max_f32_e32 v50, v51, v50
	v_max3_f32 v50, v50, v36, v37
	v_max3_f32 v50, v50, v38, v39
	v_max3_f32 v50, v50, v40, v41
	v_max3_f32 v50, v50, v42, v43
	v_max3_f32 v50, v50, v44, v45
	v_max3_f32 v50, v50, v46, v47
	v_max3_f32 v50, v50, v48, v49
	v_max3_f32 v50, v50, v18, v19
	v_max3_f32 v50, v50, v20, v21
	v_max3_f32 v50, v50, v22, v23
	v_max3_f32 v50, v50, v24, v25
	v_max3_f32 v50, v50, v26, v27
	v_max3_f32 v50, v50, v28, v29
	v_max3_f32 v50, v50, v30, v31
	v_max3_f32 v50, v50, v32, v33
	v_mov_b32_e32 v51, v50
	s_nop 1
	v_permlane32_swap_b32_e32 v50, v51
	v_max_f32_e32 v51, v51, v51
	v_max_f32_e32 v50, v50, v50
	v_max_f32_e32 v204, v50, v51
	v_sub_f32_e32 v34, v34, v204
	v_exp_f32_e32 v50, v34
	v_sub_f32_e32 v34, v35, v204
	v_exp_f32_e32 v51, v34
	v_sub_f32_e32 v34, v36, v204
	v_exp_f32_e32 v52, v34
	v_sub_f32_e32 v34, v37, v204
	v_exp_f32_e32 v53, v34
	v_sub_f32_e32 v34, v38, v204
	v_exp_f32_e32 v54, v34
	v_sub_f32_e32 v34, v39, v204
	v_exp_f32_e32 v55, v34
	v_sub_f32_e32 v34, v40, v204
	v_exp_f32_e32 v56, v34
	v_sub_f32_e32 v34, v41, v204
	v_exp_f32_e32 v57, v34
	v_sub_f32_e32 v34, v42, v204
	v_mov_b64_e32 v[16:17], s[22:23]
	v_exp_f32_e32 v58, v34
	v_sub_f32_e32 v34, v43, v204
	v_sub_f32_e32 v67, v19, v204
	s_add_i32 s8, s53, 0
	v_bfe_u32 v19, v86, 1, 5
	v_exp_f32_e32 v59, v34
	v_sub_f32_e32 v34, v44, v204
	v_sub_f32_e32 v68, v20, v204
	s_add_i32 s8, s8, 0x1e800
	v_and_b32_e32 v20, 28, v19
	s_or_b32 s10, s52, s2
	v_exp_f32_e32 v60, v34
	v_sub_f32_e32 v34, v45, v204
	v_sub_f32_e32 v69, v21, v204
	v_add_u32_e32 v201, s8, v20
	v_mov_b32_e32 v21, s8
	s_lshl_b32 s8, s54, 10
	s_ashr_i32 s11, s10, 31
	v_exp_f32_e32 v61, v34
	v_sub_f32_e32 v34, v46, v204
	s_add_i32 s89, s8, 0xf7f80000
	s_lshl_b64 s[12:13], s[10:11], 19
	v_exp_f32_e32 v62, v34
	v_sub_f32_e32 v34, v47, v204
	v_sub_f32_e32 v66, v18, v204
	v_lshrrev_b32_e32 v18, 2, v86
	s_add_u32 s12, s50, s12
	v_exp_f32_e32 v63, v34
	v_sub_f32_e32 v34, v48, v204
	v_sub_f32_e32 v70, v22, v204
	v_and_b32_e32 v128, 14, v18
	v_lshrrev_b32_e32 v22, 3, v86
	v_and_b32_e32 v18, 12, v18
	s_addc_u32 s13, s51, s13
	s_mul_i32 s8, s10, 0xc0000
	v_exp_f32_e32 v64, v34
	v_sub_f32_e32 v34, v49, v204
	v_mad_u32_u24 v199, v19, s78, v21
	v_and_b32_e32 v19, 0x80, v92
	v_and_b32_e32 v21, 16, v94
	v_and_b32_e32 v22, 4, v22
	v_and_or_b32 v198, v93, s77, v18
	v_or_b32_e32 v18, s61, v87
	s_mul_hi_i32 s2, s10, 0xc0000
	s_add_u32 s6, s6, s8
	v_exp_f32_e32 v65, v34
	v_or3_b32 v197, v19, v22, v21
	v_or3_b32 v18, v18, v88, v89
	v_mov_b32_e32 v19, v175
	s_addc_u32 s2, s7, s2
	v_and_b32_e32 v20, 1, v86
	v_lshl_add_u64 v[18:19], s[12:13], 0, v[18:19]
	s_add_u32 s6, s6, 0xc000
	v_xor_b32_e32 v34, 0x80000000, v204
	v_sub_f32_e32 v81, v33, v204
	v_sub_f32_e32 v80, v32, v204
	v_sub_f32_e32 v79, v31, v204
	v_sub_f32_e32 v78, v30, v204
	v_sub_f32_e32 v77, v29, v204
	v_sub_f32_e32 v76, v28, v204
	v_sub_f32_e32 v75, v27, v204
	v_sub_f32_e32 v74, v26, v204
	v_sub_f32_e32 v73, v25, v204
	v_sub_f32_e32 v72, v24, v204
	v_sub_f32_e32 v71, v23, v204
	v_lshlrev_b32_e32 v200, 5, v20
	v_lshlrev_b32_e32 v180, 4, v20
	v_lshl_add_u64 v[116:117], v[18:19], 0, s[46:47]
	s_addc_u32 s7, s2, 0
	v_mov_b64_e32 v[32:33], v[16:17]
	v_mov_b32_e32 v35, v34
	v_mov_b32_e32 v36, v34
	v_mov_b32_e32 v37, v34
	v_mov_b32_e32 v38, v34
	v_mov_b32_e32 v39, v34
	v_mov_b32_e32 v40, v34
	v_mov_b32_e32 v41, v34
	v_mov_b32_e32 v42, v34
	v_mov_b32_e32 v43, v34
	v_mov_b32_e32 v44, v34
	v_mov_b32_e32 v45, v34
	v_mov_b32_e32 v46, v34
	v_mov_b32_e32 v47, v34
	v_mov_b32_e32 v48, v34
	v_mov_b32_e32 v49, v34
	v_mov_b32_e32 v118, v174
	v_mov_b32_e32 v120, v82
	v_mov_b32_e32 v122, v84
	s_mov_b64 s[12:13], s[6:7]
	s_add_u32 s67, s6, 0xb4000
	v_mov_b64_e32 v[30:31], v[14:15]
	v_mov_b64_e32 v[28:29], v[12:13]
	v_mov_b64_e32 v[26:27], v[10:11]
	v_mov_b64_e32 v[24:25], v[8:9]
	v_mov_b64_e32 v[22:23], v[6:7]
	v_mov_b64_e32 v[20:21], v[4:5]
	v_mov_b64_e32 v[18:19], v[2:3]
	s_mov_b32 s6, 2
	s_mov_b32 s61, 1

; #define VM0() asm volatile("s_waitcnt vmcnt(0)" ::: "memory")
; #define B_RESC(a, rare) do { if (rare) { if (hi == 0) al_l[r32] = (a); asm volatile("s_waitcnt lgkmcnt(0)" ::: "memory"); __builtin_amdgcn_wave_barrier(); \
;         _Pragma("unroll") for (int _d = 0; _d < 2; ++_d) _Pragma("unroll") for (int _r = 0; _r < 16; ++_r) o[_d][_r] *= al_l[crow(_r, hi)]; C_SPLAT(); } } while (0)
; DEVI void attn_unit8(const Params& p, char* smem, int unit, int l, int& cvs  , CvRun& crun) {
;     ...
;     for (int T = 0; T + 1 < NTILE; ++T) {
;         const char* Kb = K_lds + s0 * 24576; const int vb = vb0 + s0 * 16384;
;         CvRegs cvr; cv_issue(p, l, cvs, lane, cvr, crun); cvs += (int)gridDim.x * 8;
;         qkt(pB0, pB1, Kb + 12288, qr, r32, hi, cinit);
;         finishSM(pA0, pA1, alA, l_reg, pa0, pa1, pa2, pa3);
;         pv_both(o[0], o[1], vb, pa0, pa1, pa2, pa3);
;         { const bool rr_ = partialSM<false>(pB0, pB1, m_reg, alB); B_RESC(alB, rr_); }
;         cv_finish(smem + 124928 + wid * 2304, lane, cvr);
;         if (cvr.live) asm volatile("s_waitcnt vmcnt(2)" ::: "memory"); else VM0();
;         __syncthreads();
;         if (T + 2 < NTILE) B_DMA(T + 2, s2);
.LBB0_2266:
	s_mul_i32 s98, s61, 0x6000
	s_add_i32 s98, s96, s98
	s_lshl_b32 s99, s61, 14
	s_add_i32 s99, s97, s99
	s_mul_i32 s6, s2, 0x6000
	s_add_i32 s6, s6, 0
	v_add_u32_e32 v249, s6, v129

; #define VM0() asm volatile("s_waitcnt vmcnt(0)" ::: "memory")
; DEVI void attn_unit8(const Params& p, char* smem, int unit, int l, int& cvs  , CvRun& crun) {
;     ...
;         if (cvr.live) asm volatile("s_waitcnt vmcnt(2)" ::: "memory"); else VM0();
;         __syncthreads();
;         if (T + 2 < NTILE) B_DMA(T + 2, s2);
;         qkt(pA0, pA1, K_lds + s1 * 24576, qr, r32, hi, cinit);
	s_mov_b32 m0, s98
	s_barrier
	ds_read_b128 v[234:237], v249
	ds_read_b128 v[212:215], v249 offset:6144
	global_load_lds_dwordx4 v118, s[12:13]
	s_waitcnt lgkmcnt(1)
	v_mfma_f32_32x32x16_bf16 v[98:113], v[234:237], v[150:153], v[34:49]
	s_add_i32 m0, s98, 0x2000

; DEVI void attn_unit8(const Params& p, char* smem, int unit, int l, int& cvs  , CvRun& crun) {
;     ...
;         if (T + 2 < NTILE) B_DMA(T + 2, s2);
;         qkt(pA0, pA1, K_lds + s1 * 24576, qr, r32, hi, cinit);
	v_add_u32_e32 v126, s6, v184
	global_load_lds_dwordx4 v120, s[12:13]
	s_waitcnt lgkmcnt(0)
	v_mfma_f32_32x32x16_bf16 v[66:81], v[212:215], v[150:153], v[34:49]
	ds_read_b128 v[212:215], v126
	ds_read_b128 v[216:219], v126 offset:6144
	s_add_i32 m0, s98, 0x4000

; template <int OFF> DEVI s16x4 tr_read(int vb) { s16x4 r; asm volatile("ds_read_b64_tr_b16 %0, %1 offset:%2" : "=&v"(r) : "v"(vb), "i"(OFF) : "memory"); return r; }
; #define SBAR() __builtin_amdgcn_sched_barrier(0)
; DEVI void pv_both(f32x16& o0, f32x16& o1, int vb, bf16x8 pa0, bf16x8 pa1, bf16x8 pa2, bf16x8 pa3) {
;     const s16x4 a0 = tr_read<v_rd_off(0, 0, 0)>(vb), b0 = tr_read<v_rd_off(0, 0, 1)>(vb), a1 = tr_read<v_rd_off(0, 1, 0)>(vb), b1 = tr_read<v_rd_off(0, 1, 1)>(vb);
;     const s16x4 a2 = tr_read<v_rd_off(0, 2, 0)>(vb), b2 = tr_read<v_rd_off(0, 2, 1)>(vb), a3 = tr_read<v_rd_off(0, 3, 0)>(vb), b3 = tr_read<v_rd_off(0, 3, 1)>(vb);
;     const s16x4 c0 = tr_read<v_rd_off(1, 0, 0)>(vb), d0 = tr_read<v_rd_off(1, 0, 1)>(vb), c1 = tr_read<v_rd_off(1, 1, 0)>(vb), d1 = tr_read<v_rd_off(1, 1, 1)>(vb);
;     const s16x4 c2 = tr_read<v_rd_off(1, 2, 0)>(vb), d2 = tr_read<v_rd_off(1, 2, 1)>(vb), c3 = tr_read<v_rd_off(1, 3, 0)>(vb), d3 = tr_read<v_rd_off(1, 3, 1)>(vb);
;     asm volatile("s_waitcnt lgkmcnt(8)" ::: "memory"); SBAR();
; DEVI void finishSM(f32x16& p0, f32x16& p1, float alpha, float& l_reg, bf16x8& pa0, bf16x8& pa1, bf16x8& pa2, bf16x8& pa3) {
; #pragma unroll
;     for (int r = 0; r < 16; ++r) p1[r] = __builtin_amdgcn_exp2f(p1[r]);
;     f32x2 s2 = (f32x2){p0[0], p0[1]} + (f32x2){p1[0], p1[1]};
; #pragma unroll
;     for (int r = 2; r < 16; r += 2) s2 += (f32x2){p0[r], p0[r + 1]} + (f32x2){p1[r], p1[r + 1]};
;     float ps = s2[0] + s2[1];
;     { auto rr = __builtin_amdgcn_permlane32_swap(__float_as_uint(ps), __float_as_uint(ps), false, false);
;       ps = __uint_as_float(rr[0]) + __uint_as_float(rr[1]); }
;     l_reg = l_reg * alpha + ps;
;     ...
;     PK4(p0, 0, pa0); PK4(p0, 8, pa1); PK4(p1, 0, pa2); PK4(p1, 8, pa3);
;     ...
; }
; DEVI void qkt(f32x16& p0, f32x16& p1, const char* Kb, const bf16x8 (&qr)[6], int r32, int hi, const f32x16& cinit) {
; #pragma unroll
;     for (int d0 = 0; d0 < 6; ++d0) { const int cb = (d0 * 16 + hi * 8) * 2;
;         const bf16x8 k0 = *(const bf16x8*)(Kb + KSWZ(r32, cb)), k1 = *(const bf16x8*)(Kb + KSWZ(32 + r32, cb));
;         p0 = __builtin_amdgcn_mfma_f32_32x32x16_bf16(k0, qr[d0], d0 == 0 ? cinit : p0, 0, 0, 0);
;         p1 = __builtin_amdgcn_mfma_f32_32x32x16_bf16(k1, qr[d0], d0 == 0 ? cinit : p1, 0, 0, 0); }
; }
	v_add_u32_e32 v126, s6, v185
	global_load_lds_dwordx4 v122, s[12:13]
	s_waitcnt lgkmcnt(1)
	v_mfma_f32_32x32x16_bf16 v[98:113], v[212:215], v[138:141], v[98:113]
	s_mov_b32 m0, s99
	v_lshl_add_u64 v[250:251], v[116:117], 0, s[40:41]
	global_load_lds_dwordx4 v[116:117], off
	s_add_i32 m0, s99, 0x2000
	v_add_u32_e32 v174, 0x2000, v203
	global_load_lds_dwordx4 v[250:251], off
	s_waitcnt lgkmcnt(0)
	v_mfma_f32_32x32x16_bf16 v[66:81], v[216:219], v[138:141], v[66:81]
	ds_read_b128 v[212:215], v126
	ds_read_b128 v[216:219], v126 offset:6144
	v_add_u32_e32 v126, s6, v205
	s_waitcnt lgkmcnt(1)
	v_mfma_f32_32x32x16_bf16 v[98:113], v[212:215], v[134:137], v[98:113]
	ds_read_b128 v[212:215], v126
	ds_read_b128 v[220:223], v126 offset:6144
	v_add_u32_e32 v126, s6, v206
	s_waitcnt lgkmcnt(2)
	v_mfma_f32_32x32x16_bf16 v[66:81], v[216:219], v[134:137], v[66:81]
	ds_read_b128 v[216:219], v126
	ds_read_b128 v[224:227], v126 offset:6144
	v_add_u32_e32 v126, s6, v207
	ds_read_b128 v[228:231], v126
	ds_read_b128 v[232:235], v126 offset:6144
	v_add_f32_e32 v126, v50, v82
	v_add_f32_e32 v127, v51, v83
	v_cvt_pk_bf16_f32 v50, v50, v51
	v_cvt_pk_bf16_f32 v51, v52, v53
	s_waitcnt lgkmcnt(5)
	v_mfma_f32_32x32x16_bf16 v[98:113], v[212:215], v[130:133], v[98:113]
	v_add_f32_e64 v212, v52, v84
	v_add_f32_e64 v213, v53, v85
	v_cvt_pk_bf16_f32 v52, v54, v55
	v_cvt_pk_bf16_f32 v53, v56, v57
	v_add_f32_e64 v126, v212, v126
	v_add_f32_e64 v127, v213, v127
	v_add_f32_e64 v212, v54, v86
	v_add_f32_e64 v213, v55, v87
	v_cvt_pk_bf16_f32 v54, v58, v59
	s_waitcnt lgkmcnt(4)
	v_mfma_f32_32x32x16_bf16 v[66:81], v[220:223], v[130:133], v[66:81]
	v_add_f32_e64 v126, v212, v126
	v_add_f32_e64 v127, v213, v127
	v_add_f32_e64 v212, v56, v88
	v_add_f32_e64 v213, v57, v89
	v_cvt_pk_bf16_f32 v55, v60, v61
	v_cvt_pk_bf16_f32 v56, v62, v63
	v_cvt_pk_bf16_f32 v57, v64, v65
	v_add_f32_e64 v126, v212, v126
	v_add_f32_e64 v127, v213, v127
	v_add_f32_e32 v212, v58, v90
	v_add_f32_e32 v213, v59, v91
	v_cvt_pk_bf16_f32 v58, v82, v83
	v_cvt_pk_bf16_f32 v59, v84, v85
	s_waitcnt lgkmcnt(3)
	v_mfma_f32_32x32x16_bf16 v[98:113], v[216:219], v[146:149], v[98:113]
	v_add_f32_e64 v126, v212, v126
	v_add_f32_e64 v127, v213, v127
	v_add_f32_e64 v212, v60, v92
	v_add_f32_e64 v213, v61, v93
	v_cvt_pk_bf16_f32 v60, v86, v87
	v_cvt_pk_bf16_f32 v61, v88, v89
	v_add_f32_e64 v126, v212, v126
	v_add_f32_e64 v127, v213, v127
	v_add_f32_e32 v212, v62, v94
	v_add_f32_e32 v213, v63, v95
	v_cvt_pk_bf16_f32 v62, v90, v91
	v_cvt_pk_bf16_f32 v63, v92, v93
	s_waitcnt lgkmcnt(2)
	v_mfma_f32_32x32x16_bf16 v[66:81], v[224:227], v[146:149], v[66:81]
	v_add_f32_e64 v126, v212, v126
	v_add_f32_e64 v127, v213, v127
	v_add_f32_e64 v212, v64, v96
	v_add_f32_e64 v213, v65, v97
	v_cvt_pk_bf16_f32 v64, v94, v95
	v_cvt_pk_bf16_f32 v65, v96, v97
	ds_read_b64_tr_b16 v[154:155], v174 offset:0
	ds_read_b64_tr_b16 v[156:157], v174 offset:0x400
	ds_read_b64_tr_b16 v[158:159], v174 offset:0x800
	ds_read_b64_tr_b16 v[160:161], v174 offset:0xc00
	ds_read_b64_tr_b16 v[162:163], v174 offset:0x1000
	ds_read_b64_tr_b16 v[164:165], v174 offset:0x1400
	ds_read_b64_tr_b16 v[166:167], v174 offset:0x1800
	ds_read_b64_tr_b16 v[168:169], v174 offset:0x1c00
	v_add_f32_e64 v126, v212, v126
	v_add_f32_e64 v127, v213, v127
	ds_read_b64_tr_b16 v[212:213], v174 offset:0x200
	ds_read_b64_tr_b16 v[214:215], v174 offset:0x600
	ds_read_b64_tr_b16 v[216:217], v174 offset:0xa00
	s_waitcnt lgkmcnt(12)
	v_mfma_f32_32x32x16_bf16 v[98:113], v[228:231], v[142:145], v[98:113]
	ds_read_b64_tr_b16 v[218:219], v174 offset:0xe00
	ds_read_b64_tr_b16 v[220:221], v174 offset:0x1200
	ds_read_b64_tr_b16 v[222:223], v174 offset:0x1600
	ds_read_b64_tr_b16 v[224:225], v174 offset:0x1a00
	ds_read_b64_tr_b16 v[226:227], v174 offset:0x1e00
	v_add_f32_e32 v126, v126, v127
	s_waitcnt lgkmcnt(15)
	v_mfma_f32_32x32x16_bf16 v[66:81], v[232:235], v[142:145], v[66:81]
	v_mov_b32_e32 v127, v126


; DEVI void pv_both(f32x16& o0, f32x16& o1, int vb, bf16x8 pa0, bf16x8 pa1, bf16x8 pa2, bf16x8 pa3) {
;     const s16x4 a0 = tr_read<v_rd_off(0, 0, 0)>(vb), b0 = tr_read<v_rd_off(0, 0, 1)>(vb), a1 = tr_read<v_rd_off(0, 1, 0)>(vb), b1 = tr_read<v_rd_off(0, 1, 1)>(vb);
;     const s16x4 a2 = tr_read<v_rd_off(0, 2, 0)>(vb), b2 = tr_read<v_rd_off(0, 2, 1)>(vb), a3 = tr_read<v_rd_off(0, 3, 0)>(vb), b3 = tr_read<v_rd_off(0, 3, 1)>(vb);
;     const s16x4 c0 = tr_read<v_rd_off(1, 0, 0)>(vb), d0 = tr_read<v_rd_off(1, 0, 1)>(vb), c1 = tr_read<v_rd_off(1, 1, 0)>(vb), d1 = tr_read<v_rd_off(1, 1, 1)>(vb);
;     const s16x4 c2 = tr_read<v_rd_off(1, 2, 0)>(vb), d2 = tr_read<v_rd_off(1, 2, 1)>(vb), c3 = tr_read<v_rd_off(1, 3, 0)>(vb), d3 = tr_read<v_rd_off(1, 3, 1)>(vb);
;     asm volatile("s_waitcnt lgkmcnt(8)" ::: "memory"); SBAR();
;     ...
;     o0 = __builtin_amdgcn_mfma_f32_32x32x16_bf16(pa0, PK(a0, b0), o0, 0, 0, 0);
;     o0 = __builtin_amdgcn_mfma_f32_32x32x16_bf16(pa1, PK(a1, b1), o0, 0, 0, 0);
;     o0 = __builtin_amdgcn_mfma_f32_32x32x16_bf16(pa2, PK(a2, b2), o0, 0, 0, 0);
;     o0 = __builtin_amdgcn_mfma_f32_32x32x16_bf16(pa3, PK(a3, b3), o0, 0, 0, 0);
;     asm volatile("s_waitcnt lgkmcnt(0)" ::: "memory"); SBAR();
;     o1 = __builtin_amdgcn_mfma_f32_32x32x16_bf16(pa0, PK(c0, d0), o1, 0, 0, 0);
;     o1 = __builtin_amdgcn_mfma_f32_32x32x16_bf16(pa1, PK(c1, d1), o1, 0, 0, 0);
;     o1 = __builtin_amdgcn_mfma_f32_32x32x16_bf16(pa2, PK(c2, d2), o1, 0, 0, 0);
;     o1 = __builtin_amdgcn_mfma_f32_32x32x16_bf16(pa3, PK(c3, d3), o1, 0, 0, 0);
;     ...
; }
; template <bool FIRST> DEVI bool partialSM(f32x16& p0, f32x16& p1, float& m_reg, float& alpha) {
;     float pmax = p0[0];
; #pragma unroll
;     for (int r = 1; r < 16; ++r) pmax = fmaxf(pmax, p0[r]);
; #pragma unroll
;     for (int r = 0; r < 16; ++r) pmax = fmaxf(pmax, p1[r]);
;     { auto rr = __builtin_amdgcn_permlane32_swap(__float_as_uint(pmax), __float_as_uint(pmax), false, false);
;       pmax = fmaxf(__uint_as_float(rr[0]), __uint_as_float(rr[1])); }
;     if (FIRST) { m_reg = pmax; alpha = 1.f;
; #pragma unroll
;         for (int r = 0; r < 16; ++r) { p0[r] = __builtin_amdgcn_exp2f(p0[r] - pmax); p1[r] = p1[r] - pmax; }
;         return false;
;     } else if (__builtin_expect(__all(pmax <= ATT_THR), 1)) { alpha = 1.f;
; #pragma unroll
;         for (int r = 0; r < 16; ++r) p0[r] = __builtin_amdgcn_exp2f(p0[r]);
	s_waitcnt lgkmcnt(14)
	v_mfma_f32_32x32x16_bf16 v[18:33], v[50:53], v[154:157], v[18:33]
	v_permlane32_swap_b32_e32 v126, v127
	s_waitcnt lgkmcnt(6)
	v_mfma_f32_32x32x16_bf16 v[2:17], v[50:53], v[212:215], v[2:17]
	s_nop 1
	v_max_f32_e32 v249, v99, v99
	v_max_f32_e32 v250, v98, v98
	v_max_f32_e32 v249, v250, v249
	v_max3_f32 v249, v249, v100, v101
	v_max3_f32 v249, v249, v102, v103
	v_max3_f32 v251, v249, v104, v105
	v_max3_f32 v251, v251, v106, v107
	v_exp_f32_e32 v50, v98
	v_exp_f32_e32 v51, v99
	v_exp_f32_e32 v52, v100
	v_exp_f32_e32 v53, v101
	v_mfma_f32_32x32x16_bf16 v[18:33], v[54:57], v[158:161], v[18:33]
	s_waitcnt lgkmcnt(4)
	v_mfma_f32_32x32x16_bf16 v[2:17], v[54:57], v[216:219], v[2:17]
	v_max3_f32 v251, v251, v108, v109
	v_max3_f32 v251, v251, v110, v111
	v_max3_f32 v251, v251, v112, v113
	v_max3_f32 v251, v251, v66, v67
	v_max3_f32 v251, v251, v68, v69
	v_max3_f32 v251, v251, v70, v71
	v_max3_f32 v251, v251, v72, v73
	v_exp_f32_e32 v54, v102
	v_exp_f32_e32 v55, v103
	v_exp_f32_e32 v56, v104
	v_exp_f32_e32 v57, v105
	v_mfma_f32_32x32x16_bf16 v[18:33], v[58:61], v[162:165], v[18:33]
	s_waitcnt lgkmcnt(2)
	v_mfma_f32_32x32x16_bf16 v[2:17], v[58:61], v[220:223], v[2:17]
	v_max3_f32 v251, v251, v74, v75
	v_max3_f32 v251, v251, v76, v77
	v_max3_f32 v251, v251, v78, v79
	v_max3_f32 v251, v251, v80, v81
	v_mov_b32_e32 v252, v251


; #define SBAR() __builtin_amdgcn_sched_barrier(0)
; DEVI void pv_both(f32x16& o0, f32x16& o1, int vb, bf16x8 pa0, bf16x8 pa1, bf16x8 pa2, bf16x8 pa3) {
;     ...
;     o0 = __builtin_amdgcn_mfma_f32_32x32x16_bf16(pa0, PK(a0, b0), o0, 0, 0, 0);
;     o0 = __builtin_amdgcn_mfma_f32_32x32x16_bf16(pa1, PK(a1, b1), o0, 0, 0, 0);
;     o0 = __builtin_amdgcn_mfma_f32_32x32x16_bf16(pa2, PK(a2, b2), o0, 0, 0, 0);
;     o0 = __builtin_amdgcn_mfma_f32_32x32x16_bf16(pa3, PK(a3, b3), o0, 0, 0, 0);
;     asm volatile("s_waitcnt lgkmcnt(0)" ::: "memory"); SBAR();
;     o1 = __builtin_amdgcn_mfma_f32_32x32x16_bf16(pa0, PK(c0, d0), o1, 0, 0, 0);
;     o1 = __builtin_amdgcn_mfma_f32_32x32x16_bf16(pa1, PK(c1, d1), o1, 0, 0, 0);
;     o1 = __builtin_amdgcn_mfma_f32_32x32x16_bf16(pa2, PK(c2, d2), o1, 0, 0, 0);
;     o1 = __builtin_amdgcn_mfma_f32_32x32x16_bf16(pa3, PK(c3, d3), o1, 0, 0, 0);
; template <bool FIRST> DEVI bool partialSM(f32x16& p0, f32x16& p1, float& m_reg, float& alpha) {
;     float pmax = p0[0];
; #pragma unroll
;     for (int r = 1; r < 16; ++r) pmax = fmaxf(pmax, p0[r]);
; #pragma unroll
;     for (int r = 0; r < 16; ++r) pmax = fmaxf(pmax, p1[r]);
;     { auto rr = __builtin_amdgcn_permlane32_swap(__float_as_uint(pmax), __float_as_uint(pmax), false, false);
;       pmax = fmaxf(__uint_as_float(rr[0]), __uint_as_float(rr[1])); }
;     if (FIRST) { m_reg = pmax; alpha = 1.f;
; #pragma unroll
;         for (int r = 0; r < 16; ++r) { p0[r] = __builtin_amdgcn_exp2f(p0[r] - pmax); p1[r] = p1[r] - pmax; }
;         return false;
;     } else if (__builtin_expect(__all(pmax <= ATT_THR), 1)) { alpha = 1.f;
; #pragma unroll
;         for (int r = 0; r < 16; ++r) p0[r] = __builtin_amdgcn_exp2f(p0[r]);
	v_exp_f32_e32 v58, v106
	v_exp_f32_e32 v59, v107
	v_permlane32_swap_b32_e32 v251, v252
	v_exp_f32_e32 v60, v108
	v_exp_f32_e32 v61, v109
	v_mfma_f32_32x32x16_bf16 v[18:33], v[62:65], v[166:169], v[18:33]
	s_waitcnt lgkmcnt(0)
	v_mfma_f32_32x32x16_bf16 v[2:17], v[62:65], v[224:227], v[2:17]
	v_exp_f32_e32 v62, v110
	v_exp_f32_e32 v63, v111
	v_exp_f32_e32 v64, v112
	v_exp_f32_e32 v65, v113
	v_max_f32_e32 v252, v252, v252
	v_max_f32_e32 v251, v251, v251
	v_max_f32_e32 v174, v251, v252
	v_cmp_ge_f32_e32 vcc, s80, v174
	s_cmp_lg_u64 vcc, exec
	s_cselect_b64 s[6:7], -1, 0
	s_cbranch_scc1 .LBB0_2275
	v_mov_b32_e32 v203, 1.0
	v_mov_b32_e32 v204, v210
	s_branch .LBB0_2280

; #define VM0() asm volatile("s_waitcnt vmcnt(0)" ::: "memory")
; #define B_RESC(a, rare) do { if (rare) { if (hi == 0) al_l[r32] = (a); asm volatile("s_waitcnt lgkmcnt(0)" ::: "memory"); __builtin_amdgcn_wave_barrier(); \
;         _Pragma("unroll") for (int _d = 0; _d < 2; ++_d) _Pragma("unroll") for (int _r = 0; _r < 16; ++_r) o[_d][_r] *= al_l[crow(_r, hi)]; C_SPLAT(); } } while (0)
; DEVI void attn_unit8(const Params& p, char* smem, int unit, int l, int& cvs  , CvRun& crun) {
;     ...
;     for (int T = 0; T + 1 < NTILE; ++T) {
;         const char* Kb = K_lds + s0 * 24576; const int vb = vb0 + s0 * 16384;
;         CvRegs cvr; cv_issue(p, l, cvs, lane, cvr, crun); cvs += (int)gridDim.x * 8;
;         qkt(pB0, pB1, Kb + 12288, qr, r32, hi, cinit);
;         finishSM(pA0, pA1, alA, l_reg, pa0, pa1, pa2, pa3);
;         pv_both(o[0], o[1], vb, pa0, pa1, pa2, pa3);
;         { const bool rr_ = partialSM<false>(pB0, pB1, m_reg, alB); B_RESC(alB, rr_); }
;         cv_finish(smem + 124928 + wid * 2304, lane, cvr);
;         if (cvr.live) asm volatile("s_waitcnt vmcnt(2)" ::: "memory"); else VM0();
;         __syncthreads();
;         if (T + 2 < NTILE) B_DMA(T + 2, s2);
;         qkt(pA0, pA1, K_lds + s1 * 24576, qr, r32, hi, cinit);
;         finishSM(pB0, pB1, alB, l_reg, pa0, pa1, pa2, pa3);
;         pv_both(o[0], o[1], vb + 8192, pa0, pa1, pa2, pa3);
;         { const bool rr_ = partialSM<false>(pA0, pA1, m_reg, alA); B_RESC(alA, rr_); }
;         { const int t = s0; s0 = s1; s1 = s2; s2 = t; }
;     }
.LBB0_2280:
	s_add_i32 s54, s54, s86
	v_add_f32_e32 v82, v124, v125
	s_add_u32 s12, s12, 0x6000
	v_fmac_f32_e32 v82, v189, v208
	v_add_f32_e32 v189, v126, v127
	s_addc_u32 s13, s13, 0
	v_fmac_f32_e32 v189, v82, v209
	s_cmp_eq_u32 s12, s67
	v_lshl_add_u64 v[116:117], v[116:117], 0, s[44:45]
	s_cbranch_scc1 .LBB0_2282
	s_mov_b32 s6, s71
	s_mov_b32 s71, s2
	v_mov_b32_e32 v208, v203
	s_branch .LBB0_2230
